# GEMM k-loops: per-segment s_setprio flips deleted, one static priority raise for waves 4-7 (the lagging half) before each k-loop, reset after it
# speedup vs baseline: 1.0267x; 1.0267x over previous
.LBB0_417:
	s_ashr_i32 s25, s24, 31
	s_lshl_b64 s[36:37], s[24:25], 21
	s_add_u32 s36, s48, s36
	s_addc_u32 s37, s49, s37
	s_and_b64 s[44:45], s[2:3], exec
	s_cselect_b32 s5, s37, s35
	s_cselect_b32 s7, s36, s34
	s_ashr_i32 s15, s14, 31
	s_lshl_b64 s[44:45], s[14:15], 21
	v_readlane_b32 s16, v254, 42
	v_readlane_b32 s17, v254, 43
	s_add_u32 s64, s16, s44
	s_addc_u32 s65, s17, s45
	s_and_b64 s[44:45], s[2:3], exec
	s_cselect_b32 s15, s65, s43
	s_cselect_b32 s25, s64, s42
	s_add_u32 s34, s34, 0x100080
	s_addc_u32 s35, s35, 0
	s_add_u32 s63, s42, 0x100
	v_mov_b32_e32 v2, 0
	s_addc_u32 s66, s43, 0
	s_mov_b32 s67, -2
	v_mov_b32_e32 v3, v2
	v_mov_b32_e32 v4, v2
	v_mov_b32_e32 v5, v2
	v_mov_b32_e32 v6, v2
	v_mov_b32_e32 v7, v2
	v_mov_b32_e32 v8, v2
	v_mov_b32_e32 v9, v2
	v_mov_b32_e32 v18, v2
	v_mov_b32_e32 v19, v2
	v_mov_b32_e32 v20, v2
	v_mov_b32_e32 v21, v2
	v_mov_b32_e32 v22, v2
	v_mov_b32_e32 v23, v2
	v_mov_b32_e32 v24, v2
	v_mov_b32_e32 v25, v2
	v_mov_b32_e32 v34, v2
	v_mov_b32_e32 v35, v2
	v_mov_b32_e32 v36, v2
	v_mov_b32_e32 v37, v2
	v_mov_b32_e32 v38, v2
	v_mov_b32_e32 v39, v2
	v_mov_b32_e32 v40, v2
	v_mov_b32_e32 v41, v2
	v_mov_b32_e32 v50, v2
	v_mov_b32_e32 v51, v2
	v_mov_b32_e32 v52, v2
	v_mov_b32_e32 v53, v2
	v_mov_b32_e32 v54, v2
	v_mov_b32_e32 v55, v2
	v_mov_b32_e32 v56, v2
	v_mov_b32_e32 v57, v2
	v_mov_b32_e32 v10, v2
	v_mov_b32_e32 v11, v2
	v_mov_b32_e32 v12, v2
	v_mov_b32_e32 v13, v2
	v_mov_b32_e32 v14, v2
	v_mov_b32_e32 v15, v2
	v_mov_b32_e32 v16, v2
	v_mov_b32_e32 v17, v2
	v_mov_b32_e32 v26, v2
	v_mov_b32_e32 v27, v2
	v_mov_b32_e32 v28, v2
	v_mov_b32_e32 v29, v2
	v_mov_b32_e32 v30, v2
	v_mov_b32_e32 v31, v2
	v_mov_b32_e32 v32, v2
	v_mov_b32_e32 v33, v2
	v_mov_b32_e32 v42, v2
	v_mov_b32_e32 v43, v2
	v_mov_b32_e32 v44, v2
	v_mov_b32_e32 v45, v2
	v_mov_b32_e32 v46, v2
	v_mov_b32_e32 v47, v2
	v_mov_b32_e32 v48, v2
	v_mov_b32_e32 v49, v2
	v_mov_b32_e32 v58, v2
	v_mov_b32_e32 v59, v2
	v_mov_b32_e32 v60, v2
	v_mov_b32_e32 v61, v2
	v_mov_b32_e32 v62, v2
	v_mov_b32_e32 v63, v2
	v_mov_b32_e32 v64, v2
	v_mov_b32_e32 v65, v2
	v_mov_b32_e32 v66, v2
	v_mov_b32_e32 v67, v2
	v_mov_b32_e32 v68, v2
	v_mov_b32_e32 v69, v2
	v_mov_b32_e32 v70, v2
	v_mov_b32_e32 v71, v2
	v_mov_b32_e32 v72, v2
	v_mov_b32_e32 v73, v2
	v_mov_b32_e32 v82, v2
	v_mov_b32_e32 v83, v2
	v_mov_b32_e32 v84, v2
	v_mov_b32_e32 v85, v2
	v_mov_b32_e32 v86, v2
	v_mov_b32_e32 v87, v2
	v_mov_b32_e32 v88, v2
	v_mov_b32_e32 v89, v2
	v_mov_b32_e32 v98, v2
	v_mov_b32_e32 v99, v2
	v_mov_b32_e32 v100, v2
	v_mov_b32_e32 v101, v2
	v_mov_b32_e32 v102, v2
	v_mov_b32_e32 v103, v2
	v_mov_b32_e32 v104, v2
	v_mov_b32_e32 v105, v2
	v_mov_b32_e32 v114, v2
	v_mov_b32_e32 v115, v2
	v_mov_b32_e32 v116, v2
	v_mov_b32_e32 v117, v2
	v_mov_b32_e32 v118, v2
	v_mov_b32_e32 v119, v2
	v_mov_b32_e32 v120, v2
	v_mov_b32_e32 v121, v2
	v_mov_b32_e32 v74, v2
	v_mov_b32_e32 v75, v2
	v_mov_b32_e32 v76, v2
	v_mov_b32_e32 v77, v2
	v_mov_b32_e32 v78, v2
	v_mov_b32_e32 v79, v2
	v_mov_b32_e32 v80, v2
	v_mov_b32_e32 v81, v2
	v_mov_b32_e32 v90, v2
	v_mov_b32_e32 v91, v2
	v_mov_b32_e32 v92, v2
	v_mov_b32_e32 v93, v2
	v_mov_b32_e32 v94, v2
	v_mov_b32_e32 v95, v2
	v_mov_b32_e32 v96, v2
	v_mov_b32_e32 v97, v2
	v_mov_b32_e32 v106, v2
	v_mov_b32_e32 v107, v2
	v_mov_b32_e32 v108, v2
	v_mov_b32_e32 v109, v2
	v_mov_b32_e32 v110, v2
	v_mov_b32_e32 v111, v2
	v_mov_b32_e32 v112, v2
	v_mov_b32_e32 v113, v2
	v_mov_b32_e32 v122, v2
	v_mov_b32_e32 v123, v2
	v_mov_b32_e32 v124, v2
	v_mov_b32_e32 v125, v2
	v_mov_b32_e32 v126, v2
	v_mov_b32_e32 v127, v2
	v_mov_b32_e32 v128, v2
	v_mov_b32_e32 v129, v2
	v_readfirstlane_b32 s38, v0
	s_nop 3
	s_lshr_b32 s38, s38, 6
	s_cmp_ge_u32 s38, 4
	s_cbranch_scc0 .Lprio_P2a
	s_setprio 1
.Lprio_P2a:
.LBB0_418:
	ds_read_b128 v[148:151], v168
	ds_read_b128 v[152:155], v168 offset:1024
	ds_read_b128 v[172:175], v168 offset:2048
	ds_read_b128 v[176:179], v168 offset:3072
	ds_read_b128 v[186:189], v169
	ds_read_b128 v[190:193], v169 offset:1024
	ds_read_b128 v[194:197], v169 offset:2048
	ds_read_b128 v[198:201], v169 offset:3072
	s_add_u32 s38, s34, 0xfff00080
	s_addc_u32 s39, s35, -1
	s_cmp_eq_u32 s67, 60
	s_cselect_b32 s45, s5, s39
	s_cselect_b32 s44, s7, s38
	s_cselect_b32 s43, s15, s66
	s_cselect_b32 s42, s25, s63
	s_add_i32 m0, s46, 0xc000
	ds_read_b128 v[202:205], v170
	ds_read_b128 v[206:209], v170 offset:1024
	ds_read_b128 v[210:213], v170 offset:2048
	ds_read_b128 v[214:217], v170 offset:3072
	ds_read_b128 v[218:221], v170 offset:4096
	ds_read_b128 v[222:225], v170 offset:5120
	ds_read_b128 v[226:229], v170 offset:6144
	ds_read_b128 v[230:233], v170 offset:7168
	global_load_lds_dwordx4 v140, s[34:35]
	s_add_i32 m0, s46, 0xe000
	s_nop 0
	global_load_lds_dwordx4 v142, s[34:35]
	s_waitcnt vmcnt(8)
	s_waitcnt lgkmcnt(0)
	s_barrier
	s_waitcnt lgkmcnt(0)
	v_mfma_f32_16x16x32_f16 v[126:129], v[148:151], v[202:205], v[126:129]
	v_mfma_f32_16x16x32_f16 v[122:125], v[172:175], v[202:205], v[122:125]
	v_mfma_f32_16x16x32_f16 v[110:113], v[148:151], v[210:213], v[110:113]
	v_mfma_f32_16x16x32_f16 v[106:109], v[172:175], v[210:213], v[106:109]
	v_mfma_f32_16x16x32_f16 v[94:97], v[148:151], v[218:221], v[94:97]
	v_mfma_f32_16x16x32_f16 v[90:93], v[172:175], v[218:221], v[90:93]
	v_mfma_f32_16x16x32_f16 v[78:81], v[148:151], v[226:229], v[78:81]
	v_mfma_f32_16x16x32_f16 v[74:77], v[172:175], v[226:229], v[74:77]
	v_mfma_f32_16x16x32_f16 v[126:129], v[152:155], v[206:209], v[126:129]
	v_mfma_f32_16x16x32_f16 v[122:125], v[176:179], v[206:209], v[122:125]
	v_mfma_f32_16x16x32_f16 v[110:113], v[152:155], v[214:217], v[110:113]
	v_mfma_f32_16x16x32_f16 v[106:109], v[176:179], v[214:217], v[106:109]
	v_mfma_f32_16x16x32_f16 v[94:97], v[152:155], v[222:225], v[94:97]
	v_mfma_f32_16x16x32_f16 v[90:93], v[176:179], v[222:225], v[90:93]
	v_mfma_f32_16x16x32_f16 v[78:81], v[152:155], v[230:233], v[78:81]
	v_mfma_f32_16x16x32_f16 v[74:77], v[176:179], v[230:233], v[74:77]
	v_mfma_f32_16x16x32_f16 v[118:121], v[186:189], v[202:205], v[118:121]
	v_mfma_f32_16x16x32_f16 v[114:117], v[194:197], v[202:205], v[114:117]
	v_mfma_f32_16x16x32_f16 v[102:105], v[186:189], v[210:213], v[102:105]
	v_mfma_f32_16x16x32_f16 v[98:101], v[194:197], v[210:213], v[98:101]
	v_mfma_f32_16x16x32_f16 v[86:89], v[186:189], v[218:221], v[86:89]
	v_mfma_f32_16x16x32_f16 v[82:85], v[194:197], v[218:221], v[82:85]
	v_mfma_f32_16x16x32_f16 v[70:73], v[186:189], v[226:229], v[70:73]
	v_mfma_f32_16x16x32_f16 v[66:69], v[194:197], v[226:229], v[66:69]
	v_mfma_f32_16x16x32_f16 v[118:121], v[190:193], v[206:209], v[118:121]
	v_mfma_f32_16x16x32_f16 v[114:117], v[198:201], v[206:209], v[114:117]
	v_mfma_f32_16x16x32_f16 v[102:105], v[190:193], v[214:217], v[102:105]
	v_mfma_f32_16x16x32_f16 v[98:101], v[198:201], v[214:217], v[98:101]
	v_mfma_f32_16x16x32_f16 v[86:89], v[190:193], v[222:225], v[86:89]
	v_mfma_f32_16x16x32_f16 v[82:85], v[198:201], v[222:225], v[82:85]
	v_mfma_f32_16x16x32_f16 v[70:73], v[190:193], v[230:233], v[70:73]
	v_mfma_f32_16x16x32_f16 v[66:69], v[198:201], v[230:233], v[66:69]
	s_barrier
	s_add_u32 s98, s42, s10
	s_addc_u32 s99, s43, s11
	s_add_u32 s100, s44, s10
	s_addc_u32 s101, s45, s11
	s_add_i32 s38, s61, s33
	s_mov_b32 m0, s38
	ds_read_b128 v[202:205], v170 offset:16384
	ds_read_b128 v[206:209], v170 offset:17408
	ds_read_b128 v[210:213], v170 offset:18432
	ds_read_b128 v[214:217], v170 offset:19456
	ds_read_b128 v[218:221], v170 offset:20480
	ds_read_b128 v[222:225], v170 offset:21504
	ds_read_b128 v[226:229], v170 offset:22528
	ds_read_b128 v[230:233], v170 offset:23552
	global_load_lds_dwordx4 v132, s[42:43]
	s_add_i32 m0, s38, 0x2000
	s_add_u32 s72, s42, 0x100000
	s_addc_u32 s73, s43, 0
	s_add_i32 s38, s62, s33
	global_load_lds_dwordx4 v136, s[42:43]
	s_mov_b32 m0, s38
	s_nop 0
	global_load_lds_dwordx4 v132, s[72:73]
	s_add_i32 m0, s38, 0x2000
	s_nop 0
	global_load_lds_dwordx4 v136, s[72:73]
	s_mov_b32 m0, s46
	s_nop 0
	global_load_lds_dwordx4 v130, s[44:45]
	s_mov_b32 m0, s47
	s_nop 0
	global_load_lds_dwordx4 v134, s[44:45]
	s_waitcnt vmcnt(8)
	s_waitcnt lgkmcnt(0)
	s_barrier
	s_waitcnt lgkmcnt(0)
	v_mfma_f32_16x16x32_f16 v[62:65], v[148:151], v[202:205], v[62:65]
	v_mfma_f32_16x16x32_f16 v[58:61], v[172:175], v[202:205], v[58:61]
	v_mfma_f32_16x16x32_f16 v[46:49], v[148:151], v[210:213], v[46:49]
	v_mfma_f32_16x16x32_f16 v[42:45], v[172:175], v[210:213], v[42:45]
	v_mfma_f32_16x16x32_f16 v[30:33], v[148:151], v[218:221], v[30:33]
	v_mfma_f32_16x16x32_f16 v[26:29], v[172:175], v[218:221], v[26:29]
	v_mfma_f32_16x16x32_f16 v[14:17], v[148:151], v[226:229], v[14:17]
	v_mfma_f32_16x16x32_f16 v[10:13], v[172:175], v[226:229], v[10:13]
	v_mfma_f32_16x16x32_f16 v[62:65], v[152:155], v[206:209], v[62:65]
	v_mfma_f32_16x16x32_f16 v[58:61], v[176:179], v[206:209], v[58:61]
	v_mfma_f32_16x16x32_f16 v[46:49], v[152:155], v[214:217], v[46:49]
	v_mfma_f32_16x16x32_f16 v[42:45], v[176:179], v[214:217], v[42:45]
	v_mfma_f32_16x16x32_f16 v[30:33], v[152:155], v[222:225], v[30:33]
	v_mfma_f32_16x16x32_f16 v[26:29], v[176:179], v[222:225], v[26:29]
	v_mfma_f32_16x16x32_f16 v[14:17], v[152:155], v[230:233], v[14:17]
	v_mfma_f32_16x16x32_f16 v[10:13], v[176:179], v[230:233], v[10:13]
	v_mfma_f32_16x16x32_f16 v[54:57], v[186:189], v[202:205], v[54:57]
	v_mfma_f32_16x16x32_f16 v[50:53], v[194:197], v[202:205], v[50:53]
	v_mfma_f32_16x16x32_f16 v[38:41], v[186:189], v[210:213], v[38:41]
	v_mfma_f32_16x16x32_f16 v[34:37], v[194:197], v[210:213], v[34:37]
	v_mfma_f32_16x16x32_f16 v[22:25], v[186:189], v[218:221], v[22:25]
	v_mfma_f32_16x16x32_f16 v[18:21], v[194:197], v[218:221], v[18:21]
	v_mfma_f32_16x16x32_f16 v[6:9], v[186:189], v[226:229], v[6:9]
	v_mfma_f32_16x16x32_f16 v[2:5], v[194:197], v[226:229], v[2:5]
	v_mfma_f32_16x16x32_f16 v[54:57], v[190:193], v[206:209], v[54:57]
	v_mfma_f32_16x16x32_f16 v[50:53], v[198:201], v[206:209], v[50:53]
	v_mfma_f32_16x16x32_f16 v[38:41], v[190:193], v[214:217], v[38:41]
	v_mfma_f32_16x16x32_f16 v[34:37], v[198:201], v[214:217], v[34:37]
	v_mfma_f32_16x16x32_f16 v[22:25], v[190:193], v[222:225], v[22:25]
	v_mfma_f32_16x16x32_f16 v[18:21], v[198:201], v[222:225], v[18:21]
	v_mfma_f32_16x16x32_f16 v[6:9], v[190:193], v[230:233], v[6:9]
	v_mfma_f32_16x16x32_f16 v[2:5], v[198:201], v[230:233], v[2:5]
	s_barrier
	s_add_i32 s38, 0, 0x18000
	v_add_u32_e32 v138, s38, v164
	s_add_i32 s39, 0, 0x1c000
	ds_read_b128 v[148:151], v138
	ds_read_b128 v[152:155], v138 offset:1024
	ds_read_b128 v[172:175], v138 offset:2048
	ds_read_b128 v[176:179], v138 offset:3072
	v_add_u32_e32 v138, s39, v164
	ds_read_b128 v[186:189], v138
	ds_read_b128 v[190:193], v138 offset:1024
	ds_read_b128 v[194:197], v138 offset:2048
	ds_read_b128 v[198:201], v138 offset:3072
	s_add_u32 s44, s44, 0x100000
	s_addc_u32 s45, s45, 0
	s_mov_b32 m0, s50
	ds_read_b128 v[202:205], v170 offset:32768
	ds_read_b128 v[206:209], v170 offset:33792
	ds_read_b128 v[210:213], v170 offset:34816
	ds_read_b128 v[214:217], v170 offset:35840
	ds_read_b128 v[218:221], v170 offset:36864
	ds_read_b128 v[222:225], v170 offset:37888
	ds_read_b128 v[226:229], v170 offset:38912
	ds_read_b128 v[230:233], v170 offset:39936
	global_load_lds_dwordx4 v130, s[44:45]
	s_mov_b32 m0, s51
	s_nop 0
	global_load_lds_dwordx4 v134, s[44:45]
	s_waitcnt vmcnt(8)
	s_waitcnt lgkmcnt(0)
	s_barrier
	s_waitcnt lgkmcnt(0)
	v_mfma_f32_16x16x32_f16 v[126:129], v[148:151], v[202:205], v[126:129]
	v_mfma_f32_16x16x32_f16 v[122:125], v[172:175], v[202:205], v[122:125]
	v_mfma_f32_16x16x32_f16 v[110:113], v[148:151], v[210:213], v[110:113]
	v_mfma_f32_16x16x32_f16 v[106:109], v[172:175], v[210:213], v[106:109]
	v_mfma_f32_16x16x32_f16 v[94:97], v[148:151], v[218:221], v[94:97]
	v_mfma_f32_16x16x32_f16 v[90:93], v[172:175], v[218:221], v[90:93]
	v_mfma_f32_16x16x32_f16 v[78:81], v[148:151], v[226:229], v[78:81]
	v_mfma_f32_16x16x32_f16 v[74:77], v[172:175], v[226:229], v[74:77]
	v_mfma_f32_16x16x32_f16 v[126:129], v[152:155], v[206:209], v[126:129]
	v_mfma_f32_16x16x32_f16 v[122:125], v[176:179], v[206:209], v[122:125]
	v_mfma_f32_16x16x32_f16 v[110:113], v[152:155], v[214:217], v[110:113]
	v_mfma_f32_16x16x32_f16 v[106:109], v[176:179], v[214:217], v[106:109]
	v_mfma_f32_16x16x32_f16 v[94:97], v[152:155], v[222:225], v[94:97]
	v_mfma_f32_16x16x32_f16 v[90:93], v[176:179], v[222:225], v[90:93]
	v_mfma_f32_16x16x32_f16 v[78:81], v[152:155], v[230:233], v[78:81]
	v_mfma_f32_16x16x32_f16 v[74:77], v[176:179], v[230:233], v[74:77]
	v_mfma_f32_16x16x32_f16 v[118:121], v[186:189], v[202:205], v[118:121]
	v_mfma_f32_16x16x32_f16 v[114:117], v[194:197], v[202:205], v[114:117]
	v_mfma_f32_16x16x32_f16 v[102:105], v[186:189], v[210:213], v[102:105]
	v_mfma_f32_16x16x32_f16 v[98:101], v[194:197], v[210:213], v[98:101]
	v_mfma_f32_16x16x32_f16 v[86:89], v[186:189], v[218:221], v[86:89]
	v_mfma_f32_16x16x32_f16 v[82:85], v[194:197], v[218:221], v[82:85]
	v_mfma_f32_16x16x32_f16 v[70:73], v[186:189], v[226:229], v[70:73]
	v_mfma_f32_16x16x32_f16 v[66:69], v[194:197], v[226:229], v[66:69]
	v_mfma_f32_16x16x32_f16 v[118:121], v[190:193], v[206:209], v[118:121]
	v_mfma_f32_16x16x32_f16 v[114:117], v[198:201], v[206:209], v[114:117]
	v_mfma_f32_16x16x32_f16 v[102:105], v[190:193], v[214:217], v[102:105]
	v_mfma_f32_16x16x32_f16 v[98:101], v[198:201], v[214:217], v[98:101]
	v_mfma_f32_16x16x32_f16 v[86:89], v[190:193], v[222:225], v[86:89]
	v_mfma_f32_16x16x32_f16 v[82:85], v[198:201], v[222:225], v[82:85]
	v_mfma_f32_16x16x32_f16 v[70:73], v[190:193], v[230:233], v[70:73]
	v_mfma_f32_16x16x32_f16 v[66:69], v[198:201], v[230:233], v[66:69]
	s_barrier
	s_add_i32 s38, s38, s33
	s_mov_b32 m0, s38
	ds_read_b128 v[202:205], v170 offset:49152
	ds_read_b128 v[206:209], v170 offset:50176
	ds_read_b128 v[210:213], v170 offset:51200
	ds_read_b128 v[214:217], v170 offset:52224
	ds_read_b128 v[218:221], v170 offset:53248
	ds_read_b128 v[222:225], v170 offset:54272
	ds_read_b128 v[226:229], v170 offset:55296
	ds_read_b128 v[230:233], v170 offset:56320
	global_load_lds_dwordx4 v132, s[98:99]
	s_add_i32 m0, s38, 0x2000
	s_add_u32 s42, s42, 0x100080
	s_addc_u32 s43, s43, 0
	s_add_i32 s38, s39, s33
	global_load_lds_dwordx4 v136, s[98:99]
	s_mov_b32 m0, s38
	s_nop 0
	global_load_lds_dwordx4 v132, s[42:43]
	s_add_i32 m0, s38, 0x2000
	s_nop 0
	global_load_lds_dwordx4 v136, s[42:43]
	s_mov_b32 m0, s53
	s_nop 0
	global_load_lds_dwordx4 v130, s[100:101]
	s_mov_b32 m0, s58
	s_nop 0
	global_load_lds_dwordx4 v134, s[100:101]
	s_waitcnt vmcnt(8)
	s_waitcnt lgkmcnt(0)
	s_barrier
	s_waitcnt lgkmcnt(0)
	v_mfma_f32_16x16x32_f16 v[62:65], v[148:151], v[202:205], v[62:65]
	v_mfma_f32_16x16x32_f16 v[58:61], v[172:175], v[202:205], v[58:61]
	v_mfma_f32_16x16x32_f16 v[46:49], v[148:151], v[210:213], v[46:49]
	v_mfma_f32_16x16x32_f16 v[42:45], v[172:175], v[210:213], v[42:45]
	v_mfma_f32_16x16x32_f16 v[30:33], v[148:151], v[218:221], v[30:33]
	v_mfma_f32_16x16x32_f16 v[26:29], v[172:175], v[218:221], v[26:29]
	v_mfma_f32_16x16x32_f16 v[14:17], v[148:151], v[226:229], v[14:17]
	v_mfma_f32_16x16x32_f16 v[10:13], v[172:175], v[226:229], v[10:13]
	v_mfma_f32_16x16x32_f16 v[62:65], v[152:155], v[206:209], v[62:65]
	v_mfma_f32_16x16x32_f16 v[58:61], v[176:179], v[206:209], v[58:61]
	v_mfma_f32_16x16x32_f16 v[46:49], v[152:155], v[214:217], v[46:49]
	v_mfma_f32_16x16x32_f16 v[42:45], v[176:179], v[214:217], v[42:45]
	v_mfma_f32_16x16x32_f16 v[30:33], v[152:155], v[222:225], v[30:33]
	v_mfma_f32_16x16x32_f16 v[26:29], v[176:179], v[222:225], v[26:29]
	v_mfma_f32_16x16x32_f16 v[14:17], v[152:155], v[230:233], v[14:17]
	v_mfma_f32_16x16x32_f16 v[10:13], v[176:179], v[230:233], v[10:13]
	v_mfma_f32_16x16x32_f16 v[54:57], v[186:189], v[202:205], v[54:57]
	v_mfma_f32_16x16x32_f16 v[50:53], v[194:197], v[202:205], v[50:53]
	v_mfma_f32_16x16x32_f16 v[38:41], v[186:189], v[210:213], v[38:41]
	v_mfma_f32_16x16x32_f16 v[34:37], v[194:197], v[210:213], v[34:37]
	v_mfma_f32_16x16x32_f16 v[22:25], v[186:189], v[218:221], v[22:25]
	v_mfma_f32_16x16x32_f16 v[18:21], v[194:197], v[218:221], v[18:21]
	v_mfma_f32_16x16x32_f16 v[6:9], v[186:189], v[226:229], v[6:9]
	v_mfma_f32_16x16x32_f16 v[2:5], v[194:197], v[226:229], v[2:5]
	v_mfma_f32_16x16x32_f16 v[54:57], v[190:193], v[206:209], v[54:57]
	v_mfma_f32_16x16x32_f16 v[50:53], v[198:201], v[206:209], v[50:53]
	v_mfma_f32_16x16x32_f16 v[38:41], v[190:193], v[214:217], v[38:41]
	v_mfma_f32_16x16x32_f16 v[34:37], v[198:201], v[214:217], v[34:37]
	v_mfma_f32_16x16x32_f16 v[22:25], v[190:193], v[222:225], v[22:25]
	v_mfma_f32_16x16x32_f16 v[18:21], v[198:201], v[222:225], v[18:21]
	v_mfma_f32_16x16x32_f16 v[6:9], v[190:193], v[230:233], v[6:9]
	v_mfma_f32_16x16x32_f16 v[2:5], v[198:201], v[230:233], v[2:5]
	s_barrier
	s_add_i32 s67, s67, 2
	s_add_u32 s34, s34, 0x100
	s_addc_u32 s35, s35, 0
	s_add_u32 s63, s63, 0x100
	s_addc_u32 s66, s66, 0
	s_cmp_gt_u32 s67, 61
	s_cbranch_scc0 .LBB0_418
	s_setprio 0
	s_and_b64 vcc, exec, s[12:13]
	s_cbranch_vccz .LBB0_421
	s_barrier

.LBB0_546:
	s_ashr_i32 s67, s66, 31
	s_lshl_b64 s[44:45], s[66:67], 20
	s_add_u32 s84, s96, s44
	s_addc_u32 s85, s97, s45
	s_and_b64 s[44:45], s[2:3], exec
	s_cselect_b32 s5, s85, s35
	s_cselect_b32 s7, s84, s34
	s_ashr_i32 s65, s64, 31
	s_lshl_b64 s[44:45], s[64:65], 20
	s_add_u32 s86, s33, s44
	s_addc_u32 s87, s46, s45
	s_and_b64 s[44:45], s[2:3], exec
	s_cselect_b32 s8, s87, s43
	s_cselect_b32 s65, s86, s42
	s_add_u32 s34, s34, 0x80080
	s_addc_u32 s35, s35, 0
	s_add_u32 s67, s42, 0x100
	v_mov_b32_e32 v2, 0
	s_addc_u32 s73, s43, 0
	s_mov_b32 s74, -2
	v_mov_b32_e32 v3, v2
	v_mov_b32_e32 v4, v2
	v_mov_b32_e32 v5, v2
	v_mov_b32_e32 v6, v2
	v_mov_b32_e32 v7, v2
	v_mov_b32_e32 v8, v2
	v_mov_b32_e32 v9, v2
	v_mov_b32_e32 v18, v2
	v_mov_b32_e32 v19, v2
	v_mov_b32_e32 v20, v2
	v_mov_b32_e32 v21, v2
	v_mov_b32_e32 v22, v2
	v_mov_b32_e32 v23, v2
	v_mov_b32_e32 v24, v2
	v_mov_b32_e32 v25, v2
	v_mov_b32_e32 v50, v2
	v_mov_b32_e32 v51, v2
	v_mov_b32_e32 v52, v2
	v_mov_b32_e32 v53, v2
	v_mov_b32_e32 v54, v2
	v_mov_b32_e32 v55, v2
	v_mov_b32_e32 v56, v2
	v_mov_b32_e32 v57, v2
	v_mov_b32_e32 v66, v2
	v_mov_b32_e32 v67, v2
	v_mov_b32_e32 v68, v2
	v_mov_b32_e32 v69, v2
	v_mov_b32_e32 v70, v2
	v_mov_b32_e32 v71, v2
	v_mov_b32_e32 v72, v2
	v_mov_b32_e32 v73, v2
	v_mov_b32_e32 v10, v2
	v_mov_b32_e32 v11, v2
	v_mov_b32_e32 v12, v2
	v_mov_b32_e32 v13, v2
	v_mov_b32_e32 v14, v2
	v_mov_b32_e32 v15, v2
	v_mov_b32_e32 v16, v2
	v_mov_b32_e32 v17, v2
	v_mov_b32_e32 v34, v2
	v_mov_b32_e32 v35, v2
	v_mov_b32_e32 v36, v2
	v_mov_b32_e32 v37, v2
	v_mov_b32_e32 v38, v2
	v_mov_b32_e32 v39, v2
	v_mov_b32_e32 v40, v2
	v_mov_b32_e32 v41, v2
	v_mov_b32_e32 v58, v2
	v_mov_b32_e32 v59, v2
	v_mov_b32_e32 v60, v2
	v_mov_b32_e32 v61, v2
	v_mov_b32_e32 v62, v2
	v_mov_b32_e32 v63, v2
	v_mov_b32_e32 v64, v2
	v_mov_b32_e32 v65, v2
	v_mov_b32_e32 v74, v2
	v_mov_b32_e32 v75, v2
	v_mov_b32_e32 v76, v2
	v_mov_b32_e32 v77, v2
	v_mov_b32_e32 v78, v2
	v_mov_b32_e32 v79, v2
	v_mov_b32_e32 v80, v2
	v_mov_b32_e32 v81, v2
	v_mov_b32_e32 v82, v2
	v_mov_b32_e32 v83, v2
	v_mov_b32_e32 v84, v2
	v_mov_b32_e32 v85, v2
	v_mov_b32_e32 v86, v2
	v_mov_b32_e32 v87, v2
	v_mov_b32_e32 v88, v2
	v_mov_b32_e32 v89, v2
	v_mov_b32_e32 v98, v2
	v_mov_b32_e32 v99, v2
	v_mov_b32_e32 v100, v2
	v_mov_b32_e32 v101, v2
	v_mov_b32_e32 v102, v2
	v_mov_b32_e32 v103, v2
	v_mov_b32_e32 v104, v2
	v_mov_b32_e32 v105, v2
	v_mov_b32_e32 v114, v2
	v_mov_b32_e32 v115, v2
	v_mov_b32_e32 v116, v2
	v_mov_b32_e32 v117, v2
	v_mov_b32_e32 v118, v2
	v_mov_b32_e32 v119, v2
	v_mov_b32_e32 v120, v2
	v_mov_b32_e32 v121, v2
	v_mov_b32_e32 v130, v2
	v_mov_b32_e32 v131, v2
	v_mov_b32_e32 v132, v2
	v_mov_b32_e32 v133, v2
	v_mov_b32_e32 v134, v2
	v_mov_b32_e32 v135, v2
	v_mov_b32_e32 v136, v2
	v_mov_b32_e32 v137, v2
	v_mov_b32_e32 v90, v2
	v_mov_b32_e32 v91, v2
	v_mov_b32_e32 v92, v2
	v_mov_b32_e32 v93, v2
	v_mov_b32_e32 v94, v2
	v_mov_b32_e32 v95, v2
	v_mov_b32_e32 v96, v2
	v_mov_b32_e32 v97, v2
	v_mov_b32_e32 v106, v2
	v_mov_b32_e32 v107, v2
	v_mov_b32_e32 v108, v2
	v_mov_b32_e32 v109, v2
	v_mov_b32_e32 v110, v2
	v_mov_b32_e32 v111, v2
	v_mov_b32_e32 v112, v2
	v_mov_b32_e32 v113, v2
	v_mov_b32_e32 v122, v2
	v_mov_b32_e32 v123, v2
	v_mov_b32_e32 v124, v2
	v_mov_b32_e32 v125, v2
	v_mov_b32_e32 v126, v2
	v_mov_b32_e32 v127, v2
	v_mov_b32_e32 v128, v2
	v_mov_b32_e32 v129, v2
	v_mov_b32_e32 v138, v2
	v_mov_b32_e32 v139, v2
	v_mov_b32_e32 v140, v2
	v_mov_b32_e32 v141, v2
	v_mov_b32_e32 v142, v2
	v_mov_b32_e32 v143, v2
	v_mov_b32_e32 v144, v2
	v_mov_b32_e32 v145, v2
	v_readfirstlane_b32 s38, v0
	s_nop 3
	s_lshr_b32 s38, s38, 6
	s_cmp_ge_u32 s38, 4
	s_cbranch_scc0 .Lprio_P2b
	s_setprio 1
.Lprio_P2b:
.LBB0_547:
	ds_read_b128 v[26:29], v191
	ds_read_b128 v[30:33], v191 offset:1024
	ds_read_b128 v[42:45], v191 offset:2048
	ds_read_b128 v[46:49], v191 offset:3072
	ds_read_b128 v[168:171], v192
	ds_read_b128 v[172:175], v192 offset:1024
	ds_read_b128 v[176:179], v192 offset:2048
	ds_read_b128 v[194:197], v192 offset:3072
	s_add_u32 s38, s34, 0xfff80080
	s_addc_u32 s39, s35, -1
	s_cmp_eq_u32 s74, 28
	s_cselect_b32 s45, s5, s39
	s_cselect_b32 s44, s7, s38
	s_cselect_b32 s43, s8, s73
	s_cselect_b32 s42, s65, s67
	s_add_i32 m0, s50, 0xc000
	ds_read_b128 v[198:201], v193
	ds_read_b128 v[202:205], v193 offset:1024
	ds_read_b128 v[206:209], v193 offset:2048
	ds_read_b128 v[210:213], v193 offset:3072
	ds_read_b128 v[214:217], v193 offset:4096
	ds_read_b128 v[218:221], v193 offset:5120
	ds_read_b128 v[222:225], v193 offset:6144
	ds_read_b128 v[226:229], v193 offset:7168
	global_load_lds_dwordx4 v156, s[34:35]
	s_add_i32 m0, s50, 0xe000
	s_nop 0
	global_load_lds_dwordx4 v158, s[34:35]
	s_waitcnt vmcnt(8)
	s_waitcnt lgkmcnt(0)
	s_barrier
	s_waitcnt lgkmcnt(0)
	v_mfma_i32_16x16x64_i8 v[142:145], v[26:29], v[198:201], v[142:145]
	v_mfma_i32_16x16x64_i8 v[138:141], v[42:45], v[198:201], v[138:141]
	v_mfma_i32_16x16x64_i8 v[126:129], v[26:29], v[206:209], v[126:129]
	v_mfma_i32_16x16x64_i8 v[122:125], v[42:45], v[206:209], v[122:125]
	v_mfma_i32_16x16x64_i8 v[110:113], v[26:29], v[214:217], v[110:113]
	v_mfma_i32_16x16x64_i8 v[106:109], v[42:45], v[214:217], v[106:109]
	v_mfma_i32_16x16x64_i8 v[94:97], v[26:29], v[222:225], v[94:97]
	v_mfma_i32_16x16x64_i8 v[90:93], v[42:45], v[222:225], v[90:93]
	v_mfma_i32_16x16x64_i8 v[142:145], v[30:33], v[202:205], v[142:145]
	v_mfma_i32_16x16x64_i8 v[138:141], v[46:49], v[202:205], v[138:141]
	v_mfma_i32_16x16x64_i8 v[126:129], v[30:33], v[210:213], v[126:129]
	v_mfma_i32_16x16x64_i8 v[122:125], v[46:49], v[210:213], v[122:125]
	v_mfma_i32_16x16x64_i8 v[110:113], v[30:33], v[218:221], v[110:113]
	v_mfma_i32_16x16x64_i8 v[106:109], v[46:49], v[218:221], v[106:109]
	v_mfma_i32_16x16x64_i8 v[94:97], v[30:33], v[226:229], v[94:97]
	v_mfma_i32_16x16x64_i8 v[90:93], v[46:49], v[226:229], v[90:93]
	v_mfma_i32_16x16x64_i8 v[134:137], v[168:171], v[198:201], v[134:137]
	v_mfma_i32_16x16x64_i8 v[130:133], v[176:179], v[198:201], v[130:133]
	v_mfma_i32_16x16x64_i8 v[118:121], v[168:171], v[206:209], v[118:121]
	v_mfma_i32_16x16x64_i8 v[114:117], v[176:179], v[206:209], v[114:117]
	v_mfma_i32_16x16x64_i8 v[102:105], v[168:171], v[214:217], v[102:105]
	v_mfma_i32_16x16x64_i8 v[98:101], v[176:179], v[214:217], v[98:101]
	v_mfma_i32_16x16x64_i8 v[86:89], v[168:171], v[222:225], v[86:89]
	v_mfma_i32_16x16x64_i8 v[82:85], v[176:179], v[222:225], v[82:85]
	v_mfma_i32_16x16x64_i8 v[134:137], v[172:175], v[202:205], v[134:137]
	v_mfma_i32_16x16x64_i8 v[130:133], v[194:197], v[202:205], v[130:133]
	v_mfma_i32_16x16x64_i8 v[118:121], v[172:175], v[210:213], v[118:121]
	v_mfma_i32_16x16x64_i8 v[114:117], v[194:197], v[210:213], v[114:117]
	v_mfma_i32_16x16x64_i8 v[102:105], v[172:175], v[218:221], v[102:105]
	v_mfma_i32_16x16x64_i8 v[98:101], v[194:197], v[218:221], v[98:101]
	v_mfma_i32_16x16x64_i8 v[86:89], v[172:175], v[226:229], v[86:89]
	v_mfma_i32_16x16x64_i8 v[82:85], v[194:197], v[226:229], v[82:85]
	s_barrier
	s_add_u32 s98, s42, s12
	s_addc_u32 s99, s43, s13
	s_add_u32 s100, s44, s12
	s_addc_u32 s101, s45, s13
	s_add_i32 s38, s62, s47
	s_mov_b32 m0, s38
	ds_read_b128 v[198:201], v193 offset:16384
	ds_read_b128 v[202:205], v193 offset:17408
	ds_read_b128 v[206:209], v193 offset:18432
	ds_read_b128 v[210:213], v193 offset:19456
	ds_read_b128 v[214:217], v193 offset:20480
	ds_read_b128 v[218:221], v193 offset:21504
	ds_read_b128 v[222:225], v193 offset:22528
	ds_read_b128 v[226:229], v193 offset:23552
	global_load_lds_dwordx4 v148, s[42:43]
	s_add_i32 m0, s38, 0x2000
	s_add_u32 s76, s42, 0x80000
	s_addc_u32 s77, s43, 0
	s_add_i32 s38, s63, s47
	global_load_lds_dwordx4 v152, s[42:43]
	s_mov_b32 m0, s38
	s_nop 0
	global_load_lds_dwordx4 v148, s[76:77]
	s_add_i32 m0, s38, 0x2000
	s_nop 0
	global_load_lds_dwordx4 v152, s[76:77]
	s_mov_b32 m0, s50
	s_nop 0
	global_load_lds_dwordx4 v146, s[44:45]
	s_mov_b32 m0, s51
	s_nop 0
	global_load_lds_dwordx4 v150, s[44:45]
	s_waitcnt vmcnt(8)
	s_waitcnt lgkmcnt(0)
	s_barrier
	s_waitcnt lgkmcnt(0)
	v_mfma_i32_16x16x64_i8 v[78:81], v[26:29], v[198:201], v[78:81]
	v_mfma_i32_16x16x64_i8 v[74:77], v[42:45], v[198:201], v[74:77]
	v_mfma_i32_16x16x64_i8 v[62:65], v[26:29], v[206:209], v[62:65]
	v_mfma_i32_16x16x64_i8 v[58:61], v[42:45], v[206:209], v[58:61]
	v_mfma_i32_16x16x64_i8 v[38:41], v[26:29], v[214:217], v[38:41]
	v_mfma_i32_16x16x64_i8 v[34:37], v[42:45], v[214:217], v[34:37]
	v_mfma_i32_16x16x64_i8 v[14:17], v[26:29], v[222:225], v[14:17]
	v_mfma_i32_16x16x64_i8 v[10:13], v[42:45], v[222:225], v[10:13]
	v_mfma_i32_16x16x64_i8 v[78:81], v[30:33], v[202:205], v[78:81]
	v_mfma_i32_16x16x64_i8 v[74:77], v[46:49], v[202:205], v[74:77]
	v_mfma_i32_16x16x64_i8 v[62:65], v[30:33], v[210:213], v[62:65]
	v_mfma_i32_16x16x64_i8 v[58:61], v[46:49], v[210:213], v[58:61]
	v_mfma_i32_16x16x64_i8 v[38:41], v[30:33], v[218:221], v[38:41]
	v_mfma_i32_16x16x64_i8 v[34:37], v[46:49], v[218:221], v[34:37]
	v_mfma_i32_16x16x64_i8 v[14:17], v[30:33], v[226:229], v[14:17]
	v_mfma_i32_16x16x64_i8 v[10:13], v[46:49], v[226:229], v[10:13]
	v_mfma_i32_16x16x64_i8 v[22:25], v[168:171], v[214:217], v[22:25]
	v_mfma_i32_16x16x64_i8 v[18:21], v[176:179], v[214:217], v[18:21]
	v_mfma_i32_16x16x64_i8 v[6:9], v[168:171], v[222:225], v[6:9]
	v_mfma_i32_16x16x64_i8 v[2:5], v[176:179], v[222:225], v[2:5]
	v_mfma_i32_16x16x64_i8 v[26:29], v[168:171], v[198:201], v[70:73]
	v_mfma_i32_16x16x64_i8 v[30:33], v[176:179], v[198:201], v[66:69]
	v_mfma_i32_16x16x64_i8 v[42:45], v[168:171], v[206:209], v[54:57]
	v_mfma_i32_16x16x64_i8 v[46:49], v[176:179], v[206:209], v[50:53]
	v_mfma_i32_16x16x64_i8 v[22:25], v[172:175], v[218:221], v[22:25]
	v_mfma_i32_16x16x64_i8 v[18:21], v[194:197], v[218:221], v[18:21]
	v_mfma_i32_16x16x64_i8 v[6:9], v[172:175], v[226:229], v[6:9]
	v_mfma_i32_16x16x64_i8 v[2:5], v[194:197], v[226:229], v[2:5]
	v_mfma_i32_16x16x64_i8 v[26:29], v[172:175], v[202:205], v[26:29]
	v_mfma_i32_16x16x64_i8 v[30:33], v[194:197], v[202:205], v[30:33]
	v_mfma_i32_16x16x64_i8 v[42:45], v[172:175], v[210:213], v[42:45]
	v_mfma_i32_16x16x64_i8 v[46:49], v[194:197], v[210:213], v[46:49]
	s_barrier
	s_add_i32 s38, 0, 0x18000
	s_add_i32 s39, 0, 0x1c000
	v_add_u32_e32 v70, s38, v188
	v_add_u32_e32 v154, s39, v188
	ds_read_b128 v[50:53], v70
	ds_read_b128 v[54:57], v70 offset:1024
	ds_read_b128 v[66:69], v70 offset:2048
	ds_read_b128 v[70:73], v70 offset:3072
	ds_read_b128 v[168:171], v154
	ds_read_b128 v[172:175], v154 offset:1024
	ds_read_b128 v[176:179], v154 offset:2048
	ds_read_b128 v[194:197], v154 offset:3072
	s_add_u32 s44, s44, 0x80000
	s_addc_u32 s45, s45, 0
	s_mov_b32 m0, s52
	ds_read_b128 v[198:201], v193 offset:32768
	ds_read_b128 v[202:205], v193 offset:33792
	ds_read_b128 v[206:209], v193 offset:34816
	ds_read_b128 v[210:213], v193 offset:35840
	ds_read_b128 v[214:217], v193 offset:36864
	ds_read_b128 v[218:221], v193 offset:37888
	ds_read_b128 v[222:225], v193 offset:38912
	ds_read_b128 v[226:229], v193 offset:39936
	global_load_lds_dwordx4 v146, s[44:45]
	s_mov_b32 m0, s53
	s_nop 0
	global_load_lds_dwordx4 v150, s[44:45]
	s_waitcnt vmcnt(8)
	s_waitcnt lgkmcnt(0)
	s_barrier
	s_waitcnt lgkmcnt(0)
	v_mfma_i32_16x16x64_i8 v[142:145], v[50:53], v[198:201], v[142:145]
	v_mfma_i32_16x16x64_i8 v[138:141], v[66:69], v[198:201], v[138:141]
	v_mfma_i32_16x16x64_i8 v[126:129], v[50:53], v[206:209], v[126:129]
	v_mfma_i32_16x16x64_i8 v[122:125], v[66:69], v[206:209], v[122:125]
	v_mfma_i32_16x16x64_i8 v[110:113], v[50:53], v[214:217], v[110:113]
	v_mfma_i32_16x16x64_i8 v[106:109], v[66:69], v[214:217], v[106:109]
	v_mfma_i32_16x16x64_i8 v[94:97], v[50:53], v[222:225], v[94:97]
	v_mfma_i32_16x16x64_i8 v[90:93], v[66:69], v[222:225], v[90:93]
	v_mfma_i32_16x16x64_i8 v[142:145], v[54:57], v[202:205], v[142:145]
	v_mfma_i32_16x16x64_i8 v[138:141], v[70:73], v[202:205], v[138:141]
	v_mfma_i32_16x16x64_i8 v[126:129], v[54:57], v[210:213], v[126:129]
	v_mfma_i32_16x16x64_i8 v[122:125], v[70:73], v[210:213], v[122:125]
	v_mfma_i32_16x16x64_i8 v[110:113], v[54:57], v[218:221], v[110:113]
	v_mfma_i32_16x16x64_i8 v[106:109], v[70:73], v[218:221], v[106:109]
	v_mfma_i32_16x16x64_i8 v[94:97], v[54:57], v[226:229], v[94:97]
	v_mfma_i32_16x16x64_i8 v[90:93], v[70:73], v[226:229], v[90:93]
	v_mfma_i32_16x16x64_i8 v[134:137], v[168:171], v[198:201], v[134:137]
	v_mfma_i32_16x16x64_i8 v[130:133], v[176:179], v[198:201], v[130:133]
	v_mfma_i32_16x16x64_i8 v[118:121], v[168:171], v[206:209], v[118:121]
	v_mfma_i32_16x16x64_i8 v[114:117], v[176:179], v[206:209], v[114:117]
	v_mfma_i32_16x16x64_i8 v[102:105], v[168:171], v[214:217], v[102:105]
	v_mfma_i32_16x16x64_i8 v[98:101], v[176:179], v[214:217], v[98:101]
	v_mfma_i32_16x16x64_i8 v[86:89], v[168:171], v[222:225], v[86:89]
	v_mfma_i32_16x16x64_i8 v[82:85], v[176:179], v[222:225], v[82:85]
	v_mfma_i32_16x16x64_i8 v[134:137], v[172:175], v[202:205], v[134:137]
	v_mfma_i32_16x16x64_i8 v[130:133], v[194:197], v[202:205], v[130:133]
	v_mfma_i32_16x16x64_i8 v[118:121], v[172:175], v[210:213], v[118:121]
	v_mfma_i32_16x16x64_i8 v[114:117], v[194:197], v[210:213], v[114:117]
	v_mfma_i32_16x16x64_i8 v[102:105], v[172:175], v[218:221], v[102:105]
	v_mfma_i32_16x16x64_i8 v[98:101], v[194:197], v[218:221], v[98:101]
	v_mfma_i32_16x16x64_i8 v[86:89], v[172:175], v[226:229], v[86:89]
	v_mfma_i32_16x16x64_i8 v[82:85], v[194:197], v[226:229], v[82:85]
	s_barrier
	s_add_i32 s38, s38, s47
	s_mov_b32 m0, s38
	ds_read_b128 v[198:201], v193 offset:49152
	ds_read_b128 v[202:205], v193 offset:50176
	ds_read_b128 v[206:209], v193 offset:51200
	ds_read_b128 v[210:213], v193 offset:52224
	ds_read_b128 v[214:217], v193 offset:53248
	ds_read_b128 v[218:221], v193 offset:54272
	ds_read_b128 v[222:225], v193 offset:55296
	ds_read_b128 v[226:229], v193 offset:56320
	global_load_lds_dwordx4 v148, s[98:99]
	s_add_i32 m0, s38, 0x2000
	s_add_u32 s42, s42, 0x80080
	s_addc_u32 s43, s43, 0
	s_add_i32 s38, s39, s47
	global_load_lds_dwordx4 v152, s[98:99]
	s_mov_b32 m0, s38
	s_nop 0
	global_load_lds_dwordx4 v148, s[42:43]
	s_add_i32 m0, s38, 0x2000
	s_nop 0
	global_load_lds_dwordx4 v152, s[42:43]
	s_mov_b32 m0, s58
	s_nop 0
	global_load_lds_dwordx4 v146, s[100:101]
	s_mov_b32 m0, s59
	s_nop 0
	global_load_lds_dwordx4 v150, s[100:101]
	s_waitcnt vmcnt(8)
	s_waitcnt lgkmcnt(0)
	s_barrier
	s_waitcnt lgkmcnt(0)
	v_mfma_i32_16x16x64_i8 v[78:81], v[50:53], v[198:201], v[78:81]
	v_mfma_i32_16x16x64_i8 v[74:77], v[66:69], v[198:201], v[74:77]
	v_mfma_i32_16x16x64_i8 v[62:65], v[50:53], v[206:209], v[62:65]
	v_mfma_i32_16x16x64_i8 v[58:61], v[66:69], v[206:209], v[58:61]
	v_mfma_i32_16x16x64_i8 v[38:41], v[50:53], v[214:217], v[38:41]
	v_mfma_i32_16x16x64_i8 v[34:37], v[66:69], v[214:217], v[34:37]
	v_mfma_i32_16x16x64_i8 v[14:17], v[50:53], v[222:225], v[14:17]
	v_mfma_i32_16x16x64_i8 v[10:13], v[66:69], v[222:225], v[10:13]
	v_mfma_i32_16x16x64_i8 v[78:81], v[54:57], v[202:205], v[78:81]
	v_mfma_i32_16x16x64_i8 v[74:77], v[70:73], v[202:205], v[74:77]
	v_mfma_i32_16x16x64_i8 v[62:65], v[54:57], v[210:213], v[62:65]
	v_mfma_i32_16x16x64_i8 v[58:61], v[70:73], v[210:213], v[58:61]
	v_mfma_i32_16x16x64_i8 v[38:41], v[54:57], v[218:221], v[38:41]
	v_mfma_i32_16x16x64_i8 v[34:37], v[70:73], v[218:221], v[34:37]
	v_mfma_i32_16x16x64_i8 v[14:17], v[54:57], v[226:229], v[14:17]
	v_mfma_i32_16x16x64_i8 v[10:13], v[70:73], v[226:229], v[10:13]
	v_mfma_i32_16x16x64_i8 v[26:29], v[168:171], v[198:201], v[26:29]
	v_mfma_i32_16x16x64_i8 v[70:73], v[172:175], v[202:205], v[26:29]
	v_mfma_i32_16x16x64_i8 v[26:29], v[176:179], v[198:201], v[30:33]
	v_mfma_i32_16x16x64_i8 v[66:69], v[194:197], v[202:205], v[26:29]
	v_mfma_i32_16x16x64_i8 v[26:29], v[168:171], v[206:209], v[42:45]
	v_mfma_i32_16x16x64_i8 v[54:57], v[172:175], v[210:213], v[26:29]
	v_mfma_i32_16x16x64_i8 v[26:29], v[176:179], v[206:209], v[46:49]
	v_mfma_i32_16x16x64_i8 v[22:25], v[168:171], v[214:217], v[22:25]
	v_mfma_i32_16x16x64_i8 v[18:21], v[176:179], v[214:217], v[18:21]
	v_mfma_i32_16x16x64_i8 v[6:9], v[168:171], v[222:225], v[6:9]
	v_mfma_i32_16x16x64_i8 v[2:5], v[176:179], v[222:225], v[2:5]
	v_mfma_i32_16x16x64_i8 v[50:53], v[194:197], v[210:213], v[26:29]
	v_mfma_i32_16x16x64_i8 v[22:25], v[172:175], v[218:221], v[22:25]
	v_mfma_i32_16x16x64_i8 v[18:21], v[194:197], v[218:221], v[18:21]
	v_mfma_i32_16x16x64_i8 v[6:9], v[172:175], v[226:229], v[6:9]
	v_mfma_i32_16x16x64_i8 v[2:5], v[194:197], v[226:229], v[2:5]
	s_barrier
	s_add_i32 s74, s74, 2
	s_add_u32 s34, s34, 0x100
	s_addc_u32 s35, s35, 0
	s_add_u32 s67, s67, 0x100
	s_addc_u32 s73, s73, 0
	s_cmp_gt_u32 s74, 29
	s_cbranch_scc0 .LBB0_547
	s_setprio 0
	s_and_b64 vcc, exec, s[14:15]
	s_cbranch_vccz .LBB0_550
	s_barrier

.LBB0_672:
	s_ashr_i32 s25, s24, 31
	s_lshl_b64 s[36:37], s[24:25], 20
	s_add_u32 s36, s50, s36
	s_addc_u32 s37, s51, s37
	s_and_b64 s[46:47], s[2:3], exec
	s_cselect_b32 s25, s37, s45
	s_cselect_b32 s73, s36, s44
	s_ashr_i32 s15, s14, 31
	s_lshl_b64 s[46:47], s[14:15], 20
	s_add_u32 s64, s96, s46
	s_addc_u32 s65, s97, s47
	s_and_b64 s[46:47], s[2:3], exec
	s_cselect_b32 s15, s65, s43
	s_cselect_b32 s74, s64, s42
	s_add_u32 s44, s44, 0x80080
	s_addc_u32 s45, s45, 0
	s_add_u32 s75, s42, 0x100
	v_mov_b32_e32 v2, 0
	s_addc_u32 s76, s43, 0
	s_mov_b32 s77, -2
	v_mov_b32_e32 v3, v2
	v_mov_b32_e32 v4, v2
	v_mov_b32_e32 v5, v2
	v_mov_b32_e32 v6, v2
	v_mov_b32_e32 v7, v2
	v_mov_b32_e32 v8, v2
	v_mov_b32_e32 v9, v2
	v_mov_b32_e32 v18, v2
	v_mov_b32_e32 v19, v2
	v_mov_b32_e32 v20, v2
	v_mov_b32_e32 v21, v2
	v_mov_b32_e32 v22, v2
	v_mov_b32_e32 v23, v2
	v_mov_b32_e32 v24, v2
	v_mov_b32_e32 v25, v2
	v_mov_b32_e32 v34, v2
	v_mov_b32_e32 v35, v2
	v_mov_b32_e32 v36, v2
	v_mov_b32_e32 v37, v2
	v_mov_b32_e32 v38, v2
	v_mov_b32_e32 v39, v2
	v_mov_b32_e32 v40, v2
	v_mov_b32_e32 v41, v2
	v_mov_b32_e32 v50, v2
	v_mov_b32_e32 v51, v2
	v_mov_b32_e32 v52, v2
	v_mov_b32_e32 v53, v2
	v_mov_b32_e32 v54, v2
	v_mov_b32_e32 v55, v2
	v_mov_b32_e32 v56, v2
	v_mov_b32_e32 v57, v2
	v_mov_b32_e32 v10, v2
	v_mov_b32_e32 v11, v2
	v_mov_b32_e32 v12, v2
	v_mov_b32_e32 v13, v2
	v_mov_b32_e32 v14, v2
	v_mov_b32_e32 v15, v2
	v_mov_b32_e32 v16, v2
	v_mov_b32_e32 v17, v2
	v_mov_b32_e32 v26, v2
	v_mov_b32_e32 v27, v2
	v_mov_b32_e32 v28, v2
	v_mov_b32_e32 v29, v2
	v_mov_b32_e32 v30, v2
	v_mov_b32_e32 v31, v2
	v_mov_b32_e32 v32, v2
	v_mov_b32_e32 v33, v2
	v_mov_b32_e32 v42, v2
	v_mov_b32_e32 v43, v2
	v_mov_b32_e32 v44, v2
	v_mov_b32_e32 v45, v2
	v_mov_b32_e32 v46, v2
	v_mov_b32_e32 v47, v2
	v_mov_b32_e32 v48, v2
	v_mov_b32_e32 v49, v2
	v_mov_b32_e32 v58, v2
	v_mov_b32_e32 v59, v2
	v_mov_b32_e32 v60, v2
	v_mov_b32_e32 v61, v2
	v_mov_b32_e32 v62, v2
	v_mov_b32_e32 v63, v2
	v_mov_b32_e32 v64, v2
	v_mov_b32_e32 v65, v2
	v_mov_b32_e32 v66, v2
	v_mov_b32_e32 v67, v2
	v_mov_b32_e32 v68, v2
	v_mov_b32_e32 v69, v2
	v_mov_b32_e32 v70, v2
	v_mov_b32_e32 v71, v2
	v_mov_b32_e32 v72, v2
	v_mov_b32_e32 v73, v2
	v_mov_b32_e32 v82, v2
	v_mov_b32_e32 v83, v2
	v_mov_b32_e32 v84, v2
	v_mov_b32_e32 v85, v2
	v_mov_b32_e32 v86, v2
	v_mov_b32_e32 v87, v2
	v_mov_b32_e32 v88, v2
	v_mov_b32_e32 v89, v2
	v_mov_b32_e32 v98, v2
	v_mov_b32_e32 v99, v2
	v_mov_b32_e32 v100, v2
	v_mov_b32_e32 v101, v2
	v_mov_b32_e32 v102, v2
	v_mov_b32_e32 v103, v2
	v_mov_b32_e32 v104, v2
	v_mov_b32_e32 v105, v2
	v_mov_b32_e32 v114, v2
	v_mov_b32_e32 v115, v2
	v_mov_b32_e32 v116, v2
	v_mov_b32_e32 v117, v2
	v_mov_b32_e32 v118, v2
	v_mov_b32_e32 v119, v2
	v_mov_b32_e32 v120, v2
	v_mov_b32_e32 v121, v2
	v_mov_b32_e32 v74, v2
	v_mov_b32_e32 v75, v2
	v_mov_b32_e32 v76, v2
	v_mov_b32_e32 v77, v2
	v_mov_b32_e32 v78, v2
	v_mov_b32_e32 v79, v2
	v_mov_b32_e32 v80, v2
	v_mov_b32_e32 v81, v2
	v_mov_b32_e32 v90, v2
	v_mov_b32_e32 v91, v2
	v_mov_b32_e32 v92, v2
	v_mov_b32_e32 v93, v2
	v_mov_b32_e32 v94, v2
	v_mov_b32_e32 v95, v2
	v_mov_b32_e32 v96, v2
	v_mov_b32_e32 v97, v2
	v_mov_b32_e32 v106, v2
	v_mov_b32_e32 v107, v2
	v_mov_b32_e32 v108, v2
	v_mov_b32_e32 v109, v2
	v_mov_b32_e32 v110, v2
	v_mov_b32_e32 v111, v2
	v_mov_b32_e32 v112, v2
	v_mov_b32_e32 v113, v2
	v_mov_b32_e32 v138, v2
	v_mov_b32_e32 v139, v2
	v_mov_b32_e32 v140, v2
	v_mov_b32_e32 v141, v2
	v_mov_b32_e32 v142, v2
	v_mov_b32_e32 v143, v2
	v_mov_b32_e32 v144, v2
	v_mov_b32_e32 v145, v2
	v_readfirstlane_b32 s38, v0
	s_nop 3
	s_lshr_b32 s38, s38, 6
	s_cmp_ge_u32 s38, 4
	s_cbranch_scc0 .Lprio_P2c
	s_setprio 1
.Lprio_P2c:
.LBB0_673:
	ds_read_b128 v[122:125], v167
	ds_read_b128 v[126:129], v167 offset:1024
	ds_read_b128 v[130:133], v167 offset:2048
	ds_read_b128 v[134:137], v167 offset:3072
	ds_read_b128 v[174:177], v171
	ds_read_b128 v[178:181], v171 offset:1024
	ds_read_b128 v[182:185], v171 offset:2048
	ds_read_b128 v[186:189], v171 offset:3072
	s_add_u32 s38, s44, 0xfff80080
	s_addc_u32 s39, s45, -1
	s_cmp_eq_u32 s77, 28
	s_cselect_b32 s47, s25, s39
	s_cselect_b32 s46, s73, s38
	s_cselect_b32 s43, s15, s76
	s_cselect_b32 s42, s74, s75
	s_add_i32 m0, s35, 0xc000
	ds_read_b128 v[190:193], v172
	ds_read_b128 v[194:197], v172 offset:1024
	ds_read_b128 v[198:201], v172 offset:2048
	ds_read_b128 v[202:205], v172 offset:3072
	ds_read_b128 v[206:209], v172 offset:4096
	ds_read_b128 v[210:213], v172 offset:5120
	ds_read_b128 v[214:217], v172 offset:6144
	ds_read_b128 v[218:221], v172 offset:7168
	global_load_lds_dwordx4 v156, s[44:45]
	s_add_i32 m0, s35, 0xe000
	s_nop 0
	global_load_lds_dwordx4 v158, s[44:45]
	s_waitcnt vmcnt(8)
	s_waitcnt lgkmcnt(0)
	s_barrier
	s_waitcnt lgkmcnt(0)
	v_mfma_i32_16x16x64_i8 v[142:145], v[122:125], v[190:193], v[142:145]
	v_mfma_i32_16x16x64_i8 v[138:141], v[130:133], v[190:193], v[138:141]
	v_mfma_i32_16x16x64_i8 v[110:113], v[122:125], v[198:201], v[110:113]
	v_mfma_i32_16x16x64_i8 v[106:109], v[130:133], v[198:201], v[106:109]
	v_mfma_i32_16x16x64_i8 v[94:97], v[122:125], v[206:209], v[94:97]
	v_mfma_i32_16x16x64_i8 v[90:93], v[130:133], v[206:209], v[90:93]
	v_mfma_i32_16x16x64_i8 v[78:81], v[122:125], v[214:217], v[78:81]
	v_mfma_i32_16x16x64_i8 v[74:77], v[130:133], v[214:217], v[74:77]
	v_mfma_i32_16x16x64_i8 v[142:145], v[126:129], v[194:197], v[142:145]
	v_mfma_i32_16x16x64_i8 v[138:141], v[134:137], v[194:197], v[138:141]
	v_mfma_i32_16x16x64_i8 v[110:113], v[126:129], v[202:205], v[110:113]
	v_mfma_i32_16x16x64_i8 v[106:109], v[134:137], v[202:205], v[106:109]
	v_mfma_i32_16x16x64_i8 v[94:97], v[126:129], v[210:213], v[94:97]
	v_mfma_i32_16x16x64_i8 v[90:93], v[134:137], v[210:213], v[90:93]
	v_mfma_i32_16x16x64_i8 v[78:81], v[126:129], v[218:221], v[78:81]
	v_mfma_i32_16x16x64_i8 v[74:77], v[134:137], v[218:221], v[74:77]
	v_mfma_i32_16x16x64_i8 v[118:121], v[174:177], v[190:193], v[118:121]
	v_mfma_i32_16x16x64_i8 v[114:117], v[182:185], v[190:193], v[114:117]
	v_mfma_i32_16x16x64_i8 v[102:105], v[174:177], v[198:201], v[102:105]
	v_mfma_i32_16x16x64_i8 v[98:101], v[182:185], v[198:201], v[98:101]
	v_mfma_i32_16x16x64_i8 v[86:89], v[174:177], v[206:209], v[86:89]
	v_mfma_i32_16x16x64_i8 v[82:85], v[182:185], v[206:209], v[82:85]
	v_mfma_i32_16x16x64_i8 v[70:73], v[174:177], v[214:217], v[70:73]
	v_mfma_i32_16x16x64_i8 v[66:69], v[182:185], v[214:217], v[66:69]
	v_mfma_i32_16x16x64_i8 v[118:121], v[178:181], v[194:197], v[118:121]
	v_mfma_i32_16x16x64_i8 v[114:117], v[186:189], v[194:197], v[114:117]
	v_mfma_i32_16x16x64_i8 v[102:105], v[178:181], v[202:205], v[102:105]
	v_mfma_i32_16x16x64_i8 v[98:101], v[186:189], v[202:205], v[98:101]
	v_mfma_i32_16x16x64_i8 v[86:89], v[178:181], v[210:213], v[86:89]
	v_mfma_i32_16x16x64_i8 v[82:85], v[186:189], v[210:213], v[82:85]
	v_mfma_i32_16x16x64_i8 v[70:73], v[178:181], v[218:221], v[70:73]
	v_mfma_i32_16x16x64_i8 v[66:69], v[186:189], v[218:221], v[66:69]
	s_barrier
	s_add_u32 s98, s42, s6
	s_addc_u32 s99, s43, s7
	s_add_u32 s100, s46, s6
	s_addc_u32 s101, s47, s7
	s_add_i32 s38, s66, s52
	s_mov_b32 m0, s38
	ds_read_b128 v[190:193], v172 offset:16384
	ds_read_b128 v[194:197], v172 offset:17408
	ds_read_b128 v[198:201], v172 offset:18432
	ds_read_b128 v[202:205], v172 offset:19456
	ds_read_b128 v[206:209], v172 offset:20480
	ds_read_b128 v[210:213], v172 offset:21504
	ds_read_b128 v[214:217], v172 offset:22528
	ds_read_b128 v[218:221], v172 offset:23552
	global_load_lds_dwordx4 v148, s[42:43]
	s_add_i32 m0, s38, 0x2000
	s_add_u32 s78, s42, 0x80000
	s_addc_u32 s79, s43, 0
	s_add_i32 s38, s67, s52
	global_load_lds_dwordx4 v152, s[42:43]
	s_mov_b32 m0, s38
	s_nop 0
	global_load_lds_dwordx4 v148, s[78:79]
	s_add_i32 m0, s38, 0x2000
	s_nop 0
	global_load_lds_dwordx4 v152, s[78:79]
	s_mov_b32 m0, s35
	s_nop 0
	global_load_lds_dwordx4 v146, s[46:47]
	s_mov_b32 m0, s53
	s_nop 0
	global_load_lds_dwordx4 v150, s[46:47]
	s_waitcnt vmcnt(8)
	s_waitcnt lgkmcnt(0)
	s_barrier
	s_waitcnt lgkmcnt(0)
	v_mfma_i32_16x16x64_i8 v[62:65], v[122:125], v[190:193], v[62:65]
	v_mfma_i32_16x16x64_i8 v[58:61], v[130:133], v[190:193], v[58:61]
	v_mfma_i32_16x16x64_i8 v[46:49], v[122:125], v[198:201], v[46:49]
	v_mfma_i32_16x16x64_i8 v[42:45], v[130:133], v[198:201], v[42:45]
	v_mfma_i32_16x16x64_i8 v[30:33], v[122:125], v[206:209], v[30:33]
	v_mfma_i32_16x16x64_i8 v[26:29], v[130:133], v[206:209], v[26:29]
	v_mfma_i32_16x16x64_i8 v[14:17], v[122:125], v[214:217], v[14:17]
	v_mfma_i32_16x16x64_i8 v[10:13], v[130:133], v[214:217], v[10:13]
	v_mfma_i32_16x16x64_i8 v[62:65], v[126:129], v[194:197], v[62:65]
	v_mfma_i32_16x16x64_i8 v[58:61], v[134:137], v[194:197], v[58:61]
	v_mfma_i32_16x16x64_i8 v[46:49], v[126:129], v[202:205], v[46:49]
	v_mfma_i32_16x16x64_i8 v[42:45], v[134:137], v[202:205], v[42:45]
	v_mfma_i32_16x16x64_i8 v[30:33], v[126:129], v[210:213], v[30:33]
	v_mfma_i32_16x16x64_i8 v[26:29], v[134:137], v[210:213], v[26:29]
	v_mfma_i32_16x16x64_i8 v[14:17], v[126:129], v[218:221], v[14:17]
	v_mfma_i32_16x16x64_i8 v[10:13], v[134:137], v[218:221], v[10:13]
	v_mfma_i32_16x16x64_i8 v[54:57], v[174:177], v[190:193], v[54:57]
	v_mfma_i32_16x16x64_i8 v[50:53], v[182:185], v[190:193], v[50:53]
	v_mfma_i32_16x16x64_i8 v[38:41], v[174:177], v[198:201], v[38:41]
	v_mfma_i32_16x16x64_i8 v[34:37], v[182:185], v[198:201], v[34:37]
	v_mfma_i32_16x16x64_i8 v[22:25], v[174:177], v[206:209], v[22:25]
	v_mfma_i32_16x16x64_i8 v[18:21], v[182:185], v[206:209], v[18:21]
	v_mfma_i32_16x16x64_i8 v[6:9], v[174:177], v[214:217], v[6:9]
	v_mfma_i32_16x16x64_i8 v[2:5], v[182:185], v[214:217], v[2:5]
	v_mfma_i32_16x16x64_i8 v[54:57], v[178:181], v[194:197], v[54:57]
	v_mfma_i32_16x16x64_i8 v[50:53], v[186:189], v[194:197], v[50:53]
	v_mfma_i32_16x16x64_i8 v[38:41], v[178:181], v[202:205], v[38:41]
	v_mfma_i32_16x16x64_i8 v[34:37], v[186:189], v[202:205], v[34:37]
	v_mfma_i32_16x16x64_i8 v[22:25], v[178:181], v[210:213], v[22:25]
	v_mfma_i32_16x16x64_i8 v[18:21], v[186:189], v[210:213], v[18:21]
	v_mfma_i32_16x16x64_i8 v[6:9], v[178:181], v[218:221], v[6:9]
	v_mfma_i32_16x16x64_i8 v[2:5], v[186:189], v[218:221], v[2:5]
	s_barrier
	s_add_i32 s38, 0, 0x18000
	s_add_i32 s39, 0, 0x1c000
	v_add_u32_e32 v134, s38, v169
	v_add_u32_e32 v154, s39, v169
	ds_read_b128 v[122:125], v134
	ds_read_b128 v[126:129], v134 offset:1024
	ds_read_b128 v[130:133], v134 offset:2048
	ds_read_b128 v[134:137], v134 offset:3072
	ds_read_b128 v[174:177], v154
	ds_read_b128 v[178:181], v154 offset:1024
	ds_read_b128 v[182:185], v154 offset:2048
	ds_read_b128 v[186:189], v154 offset:3072
	s_add_u32 s46, s46, 0x80000
	s_addc_u32 s47, s47, 0
	s_mov_b32 m0, s58
	ds_read_b128 v[190:193], v172 offset:32768
	ds_read_b128 v[194:197], v172 offset:33792
	ds_read_b128 v[198:201], v172 offset:34816
	ds_read_b128 v[202:205], v172 offset:35840
	ds_read_b128 v[206:209], v172 offset:36864
	ds_read_b128 v[210:213], v172 offset:37888
	ds_read_b128 v[214:217], v172 offset:38912
	ds_read_b128 v[218:221], v172 offset:39936
	global_load_lds_dwordx4 v146, s[46:47]
	s_mov_b32 m0, s59
	s_nop 0
	global_load_lds_dwordx4 v150, s[46:47]
	s_waitcnt vmcnt(8)
	s_waitcnt lgkmcnt(0)
	s_barrier
	s_waitcnt lgkmcnt(0)
	v_mfma_i32_16x16x64_i8 v[142:145], v[122:125], v[190:193], v[142:145]
	v_mfma_i32_16x16x64_i8 v[138:141], v[130:133], v[190:193], v[138:141]
	v_mfma_i32_16x16x64_i8 v[110:113], v[122:125], v[198:201], v[110:113]
	v_mfma_i32_16x16x64_i8 v[106:109], v[130:133], v[198:201], v[106:109]
	v_mfma_i32_16x16x64_i8 v[94:97], v[122:125], v[206:209], v[94:97]
	v_mfma_i32_16x16x64_i8 v[90:93], v[130:133], v[206:209], v[90:93]
	v_mfma_i32_16x16x64_i8 v[78:81], v[122:125], v[214:217], v[78:81]
	v_mfma_i32_16x16x64_i8 v[74:77], v[130:133], v[214:217], v[74:77]
	v_mfma_i32_16x16x64_i8 v[142:145], v[126:129], v[194:197], v[142:145]
	v_mfma_i32_16x16x64_i8 v[138:141], v[134:137], v[194:197], v[138:141]
	v_mfma_i32_16x16x64_i8 v[110:113], v[126:129], v[202:205], v[110:113]
	v_mfma_i32_16x16x64_i8 v[106:109], v[134:137], v[202:205], v[106:109]
	v_mfma_i32_16x16x64_i8 v[94:97], v[126:129], v[210:213], v[94:97]
	v_mfma_i32_16x16x64_i8 v[90:93], v[134:137], v[210:213], v[90:93]
	v_mfma_i32_16x16x64_i8 v[78:81], v[126:129], v[218:221], v[78:81]
	v_mfma_i32_16x16x64_i8 v[74:77], v[134:137], v[218:221], v[74:77]
	v_mfma_i32_16x16x64_i8 v[118:121], v[174:177], v[190:193], v[118:121]
	v_mfma_i32_16x16x64_i8 v[114:117], v[182:185], v[190:193], v[114:117]
	v_mfma_i32_16x16x64_i8 v[102:105], v[174:177], v[198:201], v[102:105]
	v_mfma_i32_16x16x64_i8 v[98:101], v[182:185], v[198:201], v[98:101]
	v_mfma_i32_16x16x64_i8 v[86:89], v[174:177], v[206:209], v[86:89]
	v_mfma_i32_16x16x64_i8 v[82:85], v[182:185], v[206:209], v[82:85]
	v_mfma_i32_16x16x64_i8 v[70:73], v[174:177], v[214:217], v[70:73]
	v_mfma_i32_16x16x64_i8 v[66:69], v[182:185], v[214:217], v[66:69]
	v_mfma_i32_16x16x64_i8 v[118:121], v[178:181], v[194:197], v[118:121]
	v_mfma_i32_16x16x64_i8 v[114:117], v[186:189], v[194:197], v[114:117]
	v_mfma_i32_16x16x64_i8 v[102:105], v[178:181], v[202:205], v[102:105]
	v_mfma_i32_16x16x64_i8 v[98:101], v[186:189], v[202:205], v[98:101]
	v_mfma_i32_16x16x64_i8 v[86:89], v[178:181], v[210:213], v[86:89]
	v_mfma_i32_16x16x64_i8 v[82:85], v[186:189], v[210:213], v[82:85]
	v_mfma_i32_16x16x64_i8 v[70:73], v[178:181], v[218:221], v[70:73]
	v_mfma_i32_16x16x64_i8 v[66:69], v[186:189], v[218:221], v[66:69]
	s_barrier
	s_add_i32 s38, s38, s52
	s_mov_b32 m0, s38
	ds_read_b128 v[190:193], v172 offset:49152
	ds_read_b128 v[194:197], v172 offset:50176
	ds_read_b128 v[198:201], v172 offset:51200
	ds_read_b128 v[202:205], v172 offset:52224
	ds_read_b128 v[206:209], v172 offset:53248
	ds_read_b128 v[210:213], v172 offset:54272
	ds_read_b128 v[214:217], v172 offset:55296
	ds_read_b128 v[218:221], v172 offset:56320
	global_load_lds_dwordx4 v148, s[98:99]
	s_add_i32 m0, s38, 0x2000
	s_add_u32 s42, s42, 0x80080
	s_addc_u32 s43, s43, 0
	s_add_i32 s38, s39, s52
	global_load_lds_dwordx4 v152, s[98:99]
	s_mov_b32 m0, s38
	s_nop 0
	global_load_lds_dwordx4 v148, s[42:43]
	s_add_i32 m0, s38, 0x2000
	s_nop 0
	global_load_lds_dwordx4 v152, s[42:43]
	s_mov_b32 m0, s61
	s_nop 0
	global_load_lds_dwordx4 v146, s[100:101]
	s_mov_b32 m0, s62
	s_nop 0
	global_load_lds_dwordx4 v150, s[100:101]
	s_waitcnt vmcnt(8)
	s_waitcnt lgkmcnt(0)
	s_barrier
	s_waitcnt lgkmcnt(0)
	v_mfma_i32_16x16x64_i8 v[62:65], v[122:125], v[190:193], v[62:65]
	v_mfma_i32_16x16x64_i8 v[58:61], v[130:133], v[190:193], v[58:61]
	v_mfma_i32_16x16x64_i8 v[46:49], v[122:125], v[198:201], v[46:49]
	v_mfma_i32_16x16x64_i8 v[42:45], v[130:133], v[198:201], v[42:45]
	v_mfma_i32_16x16x64_i8 v[30:33], v[122:125], v[206:209], v[30:33]
	v_mfma_i32_16x16x64_i8 v[26:29], v[130:133], v[206:209], v[26:29]
	v_mfma_i32_16x16x64_i8 v[14:17], v[122:125], v[214:217], v[14:17]
	v_mfma_i32_16x16x64_i8 v[10:13], v[130:133], v[214:217], v[10:13]
	v_mfma_i32_16x16x64_i8 v[62:65], v[126:129], v[194:197], v[62:65]
	v_mfma_i32_16x16x64_i8 v[58:61], v[134:137], v[194:197], v[58:61]
	v_mfma_i32_16x16x64_i8 v[46:49], v[126:129], v[202:205], v[46:49]
	v_mfma_i32_16x16x64_i8 v[42:45], v[134:137], v[202:205], v[42:45]
	v_mfma_i32_16x16x64_i8 v[30:33], v[126:129], v[210:213], v[30:33]
	v_mfma_i32_16x16x64_i8 v[26:29], v[134:137], v[210:213], v[26:29]
	v_mfma_i32_16x16x64_i8 v[14:17], v[126:129], v[218:221], v[14:17]
	v_mfma_i32_16x16x64_i8 v[10:13], v[134:137], v[218:221], v[10:13]
	v_mfma_i32_16x16x64_i8 v[54:57], v[174:177], v[190:193], v[54:57]
	v_mfma_i32_16x16x64_i8 v[50:53], v[182:185], v[190:193], v[50:53]
	v_mfma_i32_16x16x64_i8 v[38:41], v[174:177], v[198:201], v[38:41]
	v_mfma_i32_16x16x64_i8 v[34:37], v[182:185], v[198:201], v[34:37]
	v_mfma_i32_16x16x64_i8 v[22:25], v[174:177], v[206:209], v[22:25]
	v_mfma_i32_16x16x64_i8 v[18:21], v[182:185], v[206:209], v[18:21]
	v_mfma_i32_16x16x64_i8 v[6:9], v[174:177], v[214:217], v[6:9]
	v_mfma_i32_16x16x64_i8 v[2:5], v[182:185], v[214:217], v[2:5]
	v_mfma_i32_16x16x64_i8 v[54:57], v[178:181], v[194:197], v[54:57]
	v_mfma_i32_16x16x64_i8 v[50:53], v[186:189], v[194:197], v[50:53]
	v_mfma_i32_16x16x64_i8 v[38:41], v[178:181], v[202:205], v[38:41]
	v_mfma_i32_16x16x64_i8 v[34:37], v[186:189], v[202:205], v[34:37]
	v_mfma_i32_16x16x64_i8 v[22:25], v[178:181], v[210:213], v[22:25]
	v_mfma_i32_16x16x64_i8 v[18:21], v[186:189], v[210:213], v[18:21]
	v_mfma_i32_16x16x64_i8 v[6:9], v[178:181], v[218:221], v[6:9]
	v_mfma_i32_16x16x64_i8 v[2:5], v[186:189], v[218:221], v[2:5]
	s_barrier
	s_add_i32 s77, s77, 2
	s_add_u32 s44, s44, 0x100
	s_addc_u32 s45, s45, 0
	s_add_u32 s75, s75, 0x100
	s_addc_u32 s76, s76, 0
	s_cmp_gt_u32 s77, 29
	s_cbranch_scc0 .LBB0_673
	s_setprio 0
	s_and_b64 vcc, exec, s[8:9]
	s_cbranch_vccz .LBB0_676
	s_barrier

.LBB0_1488:
	s_ashr_i32 s17, s16, 31
	s_lshl_b64 s[18:19], s[16:17], 20
	s_add_u32 s18, s62, s18
	s_addc_u32 s19, s63, s19
	s_and_b64 s[20:21], s[2:3], exec
	s_cselect_b32 s17, s19, s25
	s_cselect_b32 s49, s18, s24
	s_ashr_i32 s15, s14, 31
	s_lshl_b64 s[20:21], s[14:15], 20
	s_add_u32 s20, s31, s20
	s_addc_u32 s21, s33, s21
	s_and_b64 s[28:29], s[2:3], exec
	s_cselect_b32 s15, s21, s27
	s_cselect_b32 s50, s20, s26
	s_add_u32 s24, s24, 0x80080
	s_addc_u32 s25, s25, 0
	s_add_u32 s51, s26, 0x100
	v_mov_b32_e32 v2, 0
	s_addc_u32 s52, s27, 0
	s_mov_b32 s53, -2
	v_mov_b32_e32 v3, v2
	v_mov_b32_e32 v4, v2
	v_mov_b32_e32 v5, v2
	v_mov_b32_e32 v6, v2
	v_mov_b32_e32 v7, v2
	v_mov_b32_e32 v8, v2
	v_mov_b32_e32 v9, v2
	v_mov_b32_e32 v18, v2
	v_mov_b32_e32 v19, v2
	v_mov_b32_e32 v20, v2
	v_mov_b32_e32 v21, v2
	v_mov_b32_e32 v22, v2
	v_mov_b32_e32 v23, v2
	v_mov_b32_e32 v24, v2
	v_mov_b32_e32 v25, v2
	v_mov_b32_e32 v34, v2
	v_mov_b32_e32 v35, v2
	v_mov_b32_e32 v36, v2
	v_mov_b32_e32 v37, v2
	v_mov_b32_e32 v38, v2
	v_mov_b32_e32 v39, v2
	v_mov_b32_e32 v40, v2
	v_mov_b32_e32 v41, v2
	v_mov_b32_e32 v50, v2
	v_mov_b32_e32 v51, v2
	v_mov_b32_e32 v52, v2
	v_mov_b32_e32 v53, v2
	v_mov_b32_e32 v54, v2
	v_mov_b32_e32 v55, v2
	v_mov_b32_e32 v56, v2
	v_mov_b32_e32 v57, v2
	v_mov_b32_e32 v10, v2
	v_mov_b32_e32 v11, v2
	v_mov_b32_e32 v12, v2
	v_mov_b32_e32 v13, v2
	v_mov_b32_e32 v14, v2
	v_mov_b32_e32 v15, v2
	v_mov_b32_e32 v16, v2
	v_mov_b32_e32 v17, v2
	v_mov_b32_e32 v26, v2
	v_mov_b32_e32 v27, v2
	v_mov_b32_e32 v28, v2
	v_mov_b32_e32 v29, v2
	v_mov_b32_e32 v30, v2
	v_mov_b32_e32 v31, v2
	v_mov_b32_e32 v32, v2
	v_mov_b32_e32 v33, v2
	v_mov_b32_e32 v42, v2
	v_mov_b32_e32 v43, v2
	v_mov_b32_e32 v44, v2
	v_mov_b32_e32 v45, v2
	v_mov_b32_e32 v46, v2
	v_mov_b32_e32 v47, v2
	v_mov_b32_e32 v48, v2
	v_mov_b32_e32 v49, v2
	v_mov_b32_e32 v58, v2
	v_mov_b32_e32 v59, v2
	v_mov_b32_e32 v60, v2
	v_mov_b32_e32 v61, v2
	v_mov_b32_e32 v62, v2
	v_mov_b32_e32 v63, v2
	v_mov_b32_e32 v64, v2
	v_mov_b32_e32 v65, v2
	v_mov_b32_e32 v66, v2
	v_mov_b32_e32 v67, v2
	v_mov_b32_e32 v68, v2
	v_mov_b32_e32 v69, v2
	v_mov_b32_e32 v70, v2
	v_mov_b32_e32 v71, v2
	v_mov_b32_e32 v72, v2
	v_mov_b32_e32 v73, v2
	v_mov_b32_e32 v82, v2
	v_mov_b32_e32 v83, v2
	v_mov_b32_e32 v84, v2
	v_mov_b32_e32 v85, v2
	v_mov_b32_e32 v86, v2
	v_mov_b32_e32 v87, v2
	v_mov_b32_e32 v88, v2
	v_mov_b32_e32 v89, v2
	v_mov_b32_e32 v98, v2
	v_mov_b32_e32 v99, v2
	v_mov_b32_e32 v100, v2
	v_mov_b32_e32 v101, v2
	v_mov_b32_e32 v102, v2
	v_mov_b32_e32 v103, v2
	v_mov_b32_e32 v104, v2
	v_mov_b32_e32 v105, v2
	v_mov_b32_e32 v114, v2
	v_mov_b32_e32 v115, v2
	v_mov_b32_e32 v116, v2
	v_mov_b32_e32 v117, v2
	v_mov_b32_e32 v118, v2
	v_mov_b32_e32 v119, v2
	v_mov_b32_e32 v120, v2
	v_mov_b32_e32 v121, v2
	v_mov_b32_e32 v74, v2
	v_mov_b32_e32 v75, v2
	v_mov_b32_e32 v76, v2
	v_mov_b32_e32 v77, v2
	v_mov_b32_e32 v78, v2
	v_mov_b32_e32 v79, v2
	v_mov_b32_e32 v80, v2
	v_mov_b32_e32 v81, v2
	v_mov_b32_e32 v90, v2
	v_mov_b32_e32 v91, v2
	v_mov_b32_e32 v92, v2
	v_mov_b32_e32 v93, v2
	v_mov_b32_e32 v94, v2
	v_mov_b32_e32 v95, v2
	v_mov_b32_e32 v96, v2
	v_mov_b32_e32 v97, v2
	v_mov_b32_e32 v106, v2
	v_mov_b32_e32 v107, v2
	v_mov_b32_e32 v108, v2
	v_mov_b32_e32 v109, v2
	v_mov_b32_e32 v110, v2
	v_mov_b32_e32 v111, v2
	v_mov_b32_e32 v112, v2
	v_mov_b32_e32 v113, v2
	v_mov_b32_e32 v138, v2
	v_mov_b32_e32 v139, v2
	v_mov_b32_e32 v140, v2
	v_mov_b32_e32 v141, v2
	v_mov_b32_e32 v142, v2
	v_mov_b32_e32 v143, v2
	v_mov_b32_e32 v144, v2
	v_mov_b32_e32 v145, v2
	v_readfirstlane_b32 s26, v0
	s_nop 3
	s_lshr_b32 s26, s26, 6
	s_cmp_ge_u32 s26, 4
	s_cbranch_scc0 .Lprio_P6
	s_setprio 1
.Lprio_P6:
.LBB0_1489:
	ds_read_b128 v[122:125], v169
	ds_read_b128 v[126:129], v169 offset:1024
	ds_read_b128 v[130:133], v169 offset:2048
	ds_read_b128 v[134:137], v169 offset:3072
	ds_read_b128 v[172:175], v170
	ds_read_b128 v[176:179], v170 offset:1024
	ds_read_b128 v[180:183], v170 offset:2048
	ds_read_b128 v[184:187], v170 offset:3072
	s_add_u32 s26, s24, 0xfff80080
	s_addc_u32 s27, s25, -1
	s_cmp_eq_u32 s53, 28
	s_cselect_b32 s29, s17, s27
	s_cselect_b32 s28, s49, s26
	s_cselect_b32 s27, s15, s52
	s_cselect_b32 s26, s50, s51
	s_add_i32 m0, s23, 0xc000
	ds_read_b128 v[188:191], v171
	ds_read_b128 v[192:195], v171 offset:1024
	ds_read_b128 v[196:199], v171 offset:2048
	ds_read_b128 v[200:203], v171 offset:3072
	ds_read_b128 v[204:207], v171 offset:4096
	ds_read_b128 v[208:211], v171 offset:5120
	ds_read_b128 v[212:215], v171 offset:6144
	ds_read_b128 v[216:219], v171 offset:7168
	global_load_lds_dwordx4 v156, s[24:25]
	s_add_i32 m0, s23, 0xe000
	s_nop 0
	global_load_lds_dwordx4 v158, s[24:25]
	s_waitcnt vmcnt(8)
	s_waitcnt lgkmcnt(0)
	s_barrier
	s_waitcnt lgkmcnt(0)
	v_mfma_i32_16x16x64_i8 v[142:145], v[122:125], v[188:191], v[142:145]
	v_mfma_i32_16x16x64_i8 v[138:141], v[130:133], v[188:191], v[138:141]
	v_mfma_i32_16x16x64_i8 v[110:113], v[122:125], v[196:199], v[110:113]
	v_mfma_i32_16x16x64_i8 v[106:109], v[130:133], v[196:199], v[106:109]
	v_mfma_i32_16x16x64_i8 v[94:97], v[122:125], v[204:207], v[94:97]
	v_mfma_i32_16x16x64_i8 v[90:93], v[130:133], v[204:207], v[90:93]
	v_mfma_i32_16x16x64_i8 v[78:81], v[122:125], v[212:215], v[78:81]
	v_mfma_i32_16x16x64_i8 v[74:77], v[130:133], v[212:215], v[74:77]
	v_mfma_i32_16x16x64_i8 v[142:145], v[126:129], v[192:195], v[142:145]
	v_mfma_i32_16x16x64_i8 v[138:141], v[134:137], v[192:195], v[138:141]
	v_mfma_i32_16x16x64_i8 v[110:113], v[126:129], v[200:203], v[110:113]
	v_mfma_i32_16x16x64_i8 v[106:109], v[134:137], v[200:203], v[106:109]
	v_mfma_i32_16x16x64_i8 v[94:97], v[126:129], v[208:211], v[94:97]
	v_mfma_i32_16x16x64_i8 v[90:93], v[134:137], v[208:211], v[90:93]
	v_mfma_i32_16x16x64_i8 v[78:81], v[126:129], v[216:219], v[78:81]
	v_mfma_i32_16x16x64_i8 v[74:77], v[134:137], v[216:219], v[74:77]
	v_mfma_i32_16x16x64_i8 v[118:121], v[172:175], v[188:191], v[118:121]
	v_mfma_i32_16x16x64_i8 v[114:117], v[180:183], v[188:191], v[114:117]
	v_mfma_i32_16x16x64_i8 v[102:105], v[172:175], v[196:199], v[102:105]
	v_mfma_i32_16x16x64_i8 v[98:101], v[180:183], v[196:199], v[98:101]
	v_mfma_i32_16x16x64_i8 v[86:89], v[172:175], v[204:207], v[86:89]
	v_mfma_i32_16x16x64_i8 v[82:85], v[180:183], v[204:207], v[82:85]
	v_mfma_i32_16x16x64_i8 v[70:73], v[172:175], v[212:215], v[70:73]
	v_mfma_i32_16x16x64_i8 v[66:69], v[180:183], v[212:215], v[66:69]
	v_mfma_i32_16x16x64_i8 v[118:121], v[176:179], v[192:195], v[118:121]
	v_mfma_i32_16x16x64_i8 v[114:117], v[184:187], v[192:195], v[114:117]
	v_mfma_i32_16x16x64_i8 v[102:105], v[176:179], v[200:203], v[102:105]
	v_mfma_i32_16x16x64_i8 v[98:101], v[184:187], v[200:203], v[98:101]
	v_mfma_i32_16x16x64_i8 v[86:89], v[176:179], v[208:211], v[86:89]
	v_mfma_i32_16x16x64_i8 v[82:85], v[184:187], v[208:211], v[82:85]
	v_mfma_i32_16x16x64_i8 v[70:73], v[176:179], v[216:219], v[70:73]
	v_mfma_i32_16x16x64_i8 v[66:69], v[184:187], v[216:219], v[66:69]
	s_barrier
	s_add_u32 s98, s26, s10
	s_addc_u32 s99, s27, s11
	s_add_u32 s100, s28, s10
	s_addc_u32 s101, s29, s11
	s_add_i32 s38, s46, s34
	s_mov_b32 m0, s38
	ds_read_b128 v[188:191], v171 offset:16384
	ds_read_b128 v[192:195], v171 offset:17408
	ds_read_b128 v[196:199], v171 offset:18432
	ds_read_b128 v[200:203], v171 offset:19456
	ds_read_b128 v[204:207], v171 offset:20480
	ds_read_b128 v[208:211], v171 offset:21504
	ds_read_b128 v[212:215], v171 offset:22528
	ds_read_b128 v[216:219], v171 offset:23552
	global_load_lds_dwordx4 v148, s[26:27]
	s_add_i32 m0, s38, 0x2000
	s_add_u32 s38, s26, 0x80000
	s_addc_u32 s39, s27, 0
	s_add_i32 s54, s47, s34
	global_load_lds_dwordx4 v152, s[26:27]
	s_mov_b32 m0, s54
	s_nop 0
	global_load_lds_dwordx4 v148, s[38:39]
	s_add_i32 m0, s54, 0x2000
	s_nop 0
	global_load_lds_dwordx4 v152, s[38:39]
	s_mov_b32 m0, s23
	s_nop 0
	global_load_lds_dwordx4 v146, s[28:29]
	s_mov_b32 m0, s35
	s_nop 0
	global_load_lds_dwordx4 v150, s[28:29]
	s_waitcnt vmcnt(8)
	s_waitcnt lgkmcnt(0)
	s_barrier
	s_waitcnt lgkmcnt(0)
	v_mfma_i32_16x16x64_i8 v[62:65], v[122:125], v[188:191], v[62:65]
	v_mfma_i32_16x16x64_i8 v[58:61], v[130:133], v[188:191], v[58:61]
	v_mfma_i32_16x16x64_i8 v[46:49], v[122:125], v[196:199], v[46:49]
	v_mfma_i32_16x16x64_i8 v[42:45], v[130:133], v[196:199], v[42:45]
	v_mfma_i32_16x16x64_i8 v[30:33], v[122:125], v[204:207], v[30:33]
	v_mfma_i32_16x16x64_i8 v[26:29], v[130:133], v[204:207], v[26:29]
	v_mfma_i32_16x16x64_i8 v[14:17], v[122:125], v[212:215], v[14:17]
	v_mfma_i32_16x16x64_i8 v[10:13], v[130:133], v[212:215], v[10:13]
	v_mfma_i32_16x16x64_i8 v[62:65], v[126:129], v[192:195], v[62:65]
	v_mfma_i32_16x16x64_i8 v[58:61], v[134:137], v[192:195], v[58:61]
	v_mfma_i32_16x16x64_i8 v[46:49], v[126:129], v[200:203], v[46:49]
	v_mfma_i32_16x16x64_i8 v[42:45], v[134:137], v[200:203], v[42:45]
	v_mfma_i32_16x16x64_i8 v[30:33], v[126:129], v[208:211], v[30:33]
	v_mfma_i32_16x16x64_i8 v[26:29], v[134:137], v[208:211], v[26:29]
	v_mfma_i32_16x16x64_i8 v[14:17], v[126:129], v[216:219], v[14:17]
	v_mfma_i32_16x16x64_i8 v[10:13], v[134:137], v[216:219], v[10:13]
	v_mfma_i32_16x16x64_i8 v[54:57], v[172:175], v[188:191], v[54:57]
	v_mfma_i32_16x16x64_i8 v[50:53], v[180:183], v[188:191], v[50:53]
	v_mfma_i32_16x16x64_i8 v[38:41], v[172:175], v[196:199], v[38:41]
	v_mfma_i32_16x16x64_i8 v[34:37], v[180:183], v[196:199], v[34:37]
	v_mfma_i32_16x16x64_i8 v[22:25], v[172:175], v[204:207], v[22:25]
	v_mfma_i32_16x16x64_i8 v[18:21], v[180:183], v[204:207], v[18:21]
	v_mfma_i32_16x16x64_i8 v[6:9], v[172:175], v[212:215], v[6:9]
	v_mfma_i32_16x16x64_i8 v[2:5], v[180:183], v[212:215], v[2:5]
	v_mfma_i32_16x16x64_i8 v[54:57], v[176:179], v[192:195], v[54:57]
	v_mfma_i32_16x16x64_i8 v[50:53], v[184:187], v[192:195], v[50:53]
	v_mfma_i32_16x16x64_i8 v[38:41], v[176:179], v[200:203], v[38:41]
	v_mfma_i32_16x16x64_i8 v[34:37], v[184:187], v[200:203], v[34:37]
	v_mfma_i32_16x16x64_i8 v[22:25], v[176:179], v[208:211], v[22:25]
	v_mfma_i32_16x16x64_i8 v[18:21], v[184:187], v[208:211], v[18:21]
	v_mfma_i32_16x16x64_i8 v[6:9], v[176:179], v[216:219], v[6:9]
	v_mfma_i32_16x16x64_i8 v[2:5], v[184:187], v[216:219], v[2:5]
	s_barrier
	s_add_i32 s38, 0, 0x18000
	s_add_i32 s39, 0, 0x1c000
	v_add_u32_e32 v134, s38, v167
	v_add_u32_e32 v154, s39, v167
	ds_read_b128 v[122:125], v134
	ds_read_b128 v[126:129], v134 offset:1024
	ds_read_b128 v[130:133], v134 offset:2048
	ds_read_b128 v[134:137], v134 offset:3072
	ds_read_b128 v[172:175], v154
	ds_read_b128 v[176:179], v154 offset:1024
	ds_read_b128 v[180:183], v154 offset:2048
	ds_read_b128 v[184:187], v154 offset:3072
	s_add_u32 s28, s28, 0x80000
	s_addc_u32 s29, s29, 0
	s_mov_b32 m0, s36
	ds_read_b128 v[188:191], v171 offset:32768
	ds_read_b128 v[192:195], v171 offset:33792
	ds_read_b128 v[196:199], v171 offset:34816
	ds_read_b128 v[200:203], v171 offset:35840
	ds_read_b128 v[204:207], v171 offset:36864
	ds_read_b128 v[208:211], v171 offset:37888
	ds_read_b128 v[212:215], v171 offset:38912
	ds_read_b128 v[216:219], v171 offset:39936
	global_load_lds_dwordx4 v146, s[28:29]
	s_mov_b32 m0, s37
	s_nop 0
	global_load_lds_dwordx4 v150, s[28:29]
	s_waitcnt vmcnt(8)
	s_waitcnt lgkmcnt(0)
	s_barrier
	s_waitcnt lgkmcnt(0)
	v_mfma_i32_16x16x64_i8 v[142:145], v[122:125], v[188:191], v[142:145]
	v_mfma_i32_16x16x64_i8 v[138:141], v[130:133], v[188:191], v[138:141]
	v_mfma_i32_16x16x64_i8 v[110:113], v[122:125], v[196:199], v[110:113]
	v_mfma_i32_16x16x64_i8 v[106:109], v[130:133], v[196:199], v[106:109]
	v_mfma_i32_16x16x64_i8 v[94:97], v[122:125], v[204:207], v[94:97]
	v_mfma_i32_16x16x64_i8 v[90:93], v[130:133], v[204:207], v[90:93]
	v_mfma_i32_16x16x64_i8 v[78:81], v[122:125], v[212:215], v[78:81]
	v_mfma_i32_16x16x64_i8 v[74:77], v[130:133], v[212:215], v[74:77]
	v_mfma_i32_16x16x64_i8 v[142:145], v[126:129], v[192:195], v[142:145]
	v_mfma_i32_16x16x64_i8 v[138:141], v[134:137], v[192:195], v[138:141]
	v_mfma_i32_16x16x64_i8 v[110:113], v[126:129], v[200:203], v[110:113]
	v_mfma_i32_16x16x64_i8 v[106:109], v[134:137], v[200:203], v[106:109]
	v_mfma_i32_16x16x64_i8 v[94:97], v[126:129], v[208:211], v[94:97]
	v_mfma_i32_16x16x64_i8 v[90:93], v[134:137], v[208:211], v[90:93]
	v_mfma_i32_16x16x64_i8 v[78:81], v[126:129], v[216:219], v[78:81]
	v_mfma_i32_16x16x64_i8 v[74:77], v[134:137], v[216:219], v[74:77]
	v_mfma_i32_16x16x64_i8 v[118:121], v[172:175], v[188:191], v[118:121]
	v_mfma_i32_16x16x64_i8 v[114:117], v[180:183], v[188:191], v[114:117]
	v_mfma_i32_16x16x64_i8 v[102:105], v[172:175], v[196:199], v[102:105]
	v_mfma_i32_16x16x64_i8 v[98:101], v[180:183], v[196:199], v[98:101]
	v_mfma_i32_16x16x64_i8 v[86:89], v[172:175], v[204:207], v[86:89]
	v_mfma_i32_16x16x64_i8 v[82:85], v[180:183], v[204:207], v[82:85]
	v_mfma_i32_16x16x64_i8 v[70:73], v[172:175], v[212:215], v[70:73]
	v_mfma_i32_16x16x64_i8 v[66:69], v[180:183], v[212:215], v[66:69]
	v_mfma_i32_16x16x64_i8 v[118:121], v[176:179], v[192:195], v[118:121]
	v_mfma_i32_16x16x64_i8 v[114:117], v[184:187], v[192:195], v[114:117]
	v_mfma_i32_16x16x64_i8 v[102:105], v[176:179], v[200:203], v[102:105]
	v_mfma_i32_16x16x64_i8 v[98:101], v[184:187], v[200:203], v[98:101]
	v_mfma_i32_16x16x64_i8 v[86:89], v[176:179], v[208:211], v[86:89]
	v_mfma_i32_16x16x64_i8 v[82:85], v[184:187], v[208:211], v[82:85]
	v_mfma_i32_16x16x64_i8 v[70:73], v[176:179], v[216:219], v[70:73]
	v_mfma_i32_16x16x64_i8 v[66:69], v[184:187], v[216:219], v[66:69]
	s_barrier
	s_add_i32 s28, s38, s34
	s_mov_b32 m0, s28
	ds_read_b128 v[188:191], v171 offset:49152
	ds_read_b128 v[192:195], v171 offset:50176
	ds_read_b128 v[196:199], v171 offset:51200
	ds_read_b128 v[200:203], v171 offset:52224
	ds_read_b128 v[204:207], v171 offset:53248
	ds_read_b128 v[208:211], v171 offset:54272
	ds_read_b128 v[212:215], v171 offset:55296
	ds_read_b128 v[216:219], v171 offset:56320
	global_load_lds_dwordx4 v148, s[98:99]
	s_add_i32 m0, s28, 0x2000
	s_add_u32 s26, s26, 0x80080
	s_addc_u32 s27, s27, 0
	s_add_i32 s28, s39, s34
	global_load_lds_dwordx4 v152, s[98:99]
	s_mov_b32 m0, s28
	s_nop 0
	global_load_lds_dwordx4 v148, s[26:27]
	s_add_i32 m0, s28, 0x2000
	s_nop 0
	global_load_lds_dwordx4 v152, s[26:27]
	s_mov_b32 m0, s43
	s_nop 0
	global_load_lds_dwordx4 v146, s[100:101]
	s_mov_b32 m0, s44
	s_nop 0
	global_load_lds_dwordx4 v150, s[100:101]
	s_waitcnt vmcnt(8)
	s_waitcnt lgkmcnt(0)
	s_barrier
	s_waitcnt lgkmcnt(0)
	v_mfma_i32_16x16x64_i8 v[62:65], v[122:125], v[188:191], v[62:65]
	v_mfma_i32_16x16x64_i8 v[58:61], v[130:133], v[188:191], v[58:61]
	v_mfma_i32_16x16x64_i8 v[46:49], v[122:125], v[196:199], v[46:49]
	v_mfma_i32_16x16x64_i8 v[42:45], v[130:133], v[196:199], v[42:45]
	v_mfma_i32_16x16x64_i8 v[30:33], v[122:125], v[204:207], v[30:33]
	v_mfma_i32_16x16x64_i8 v[26:29], v[130:133], v[204:207], v[26:29]
	v_mfma_i32_16x16x64_i8 v[14:17], v[122:125], v[212:215], v[14:17]
	v_mfma_i32_16x16x64_i8 v[10:13], v[130:133], v[212:215], v[10:13]
	v_mfma_i32_16x16x64_i8 v[62:65], v[126:129], v[192:195], v[62:65]
	v_mfma_i32_16x16x64_i8 v[58:61], v[134:137], v[192:195], v[58:61]
	v_mfma_i32_16x16x64_i8 v[46:49], v[126:129], v[200:203], v[46:49]
	v_mfma_i32_16x16x64_i8 v[42:45], v[134:137], v[200:203], v[42:45]
	v_mfma_i32_16x16x64_i8 v[30:33], v[126:129], v[208:211], v[30:33]
	v_mfma_i32_16x16x64_i8 v[26:29], v[134:137], v[208:211], v[26:29]
	v_mfma_i32_16x16x64_i8 v[14:17], v[126:129], v[216:219], v[14:17]
	v_mfma_i32_16x16x64_i8 v[10:13], v[134:137], v[216:219], v[10:13]
	v_mfma_i32_16x16x64_i8 v[54:57], v[172:175], v[188:191], v[54:57]
	v_mfma_i32_16x16x64_i8 v[50:53], v[180:183], v[188:191], v[50:53]
	v_mfma_i32_16x16x64_i8 v[38:41], v[172:175], v[196:199], v[38:41]
	v_mfma_i32_16x16x64_i8 v[34:37], v[180:183], v[196:199], v[34:37]
	v_mfma_i32_16x16x64_i8 v[22:25], v[172:175], v[204:207], v[22:25]
	v_mfma_i32_16x16x64_i8 v[18:21], v[180:183], v[204:207], v[18:21]
	v_mfma_i32_16x16x64_i8 v[6:9], v[172:175], v[212:215], v[6:9]
	v_mfma_i32_16x16x64_i8 v[2:5], v[180:183], v[212:215], v[2:5]
	v_mfma_i32_16x16x64_i8 v[54:57], v[176:179], v[192:195], v[54:57]
	v_mfma_i32_16x16x64_i8 v[50:53], v[184:187], v[192:195], v[50:53]
	v_mfma_i32_16x16x64_i8 v[38:41], v[176:179], v[200:203], v[38:41]
	v_mfma_i32_16x16x64_i8 v[34:37], v[184:187], v[200:203], v[34:37]
	v_mfma_i32_16x16x64_i8 v[22:25], v[176:179], v[208:211], v[22:25]
	v_mfma_i32_16x16x64_i8 v[18:21], v[184:187], v[208:211], v[18:21]
	v_mfma_i32_16x16x64_i8 v[6:9], v[176:179], v[216:219], v[6:9]
	v_mfma_i32_16x16x64_i8 v[2:5], v[184:187], v[216:219], v[2:5]
	s_barrier
	s_add_i32 s53, s53, 2
	s_add_u32 s24, s24, 0x100
	s_addc_u32 s25, s25, 0
	s_add_u32 s51, s51, 0x100
	s_addc_u32 s52, s52, 0
	s_cmp_gt_u32 s53, 29
	s_cbranch_scc0 .LBB0_1489
	s_setprio 0
	s_and_b64 vcc, exec, s[12:13]
	s_cbranch_vccz .LBB0_1492
	s_barrier

.LBB0_1648:
	s_ashr_i32 s29, s28, 31
	s_lshl_b64 s[30:31], s[28:29], 20
	v_readlane_b32 s36, v254, 42
	v_readlane_b32 s37, v254, 43
	s_add_u32 s30, s36, s30
	s_addc_u32 s31, s37, s31
	s_and_b64 s[36:37], s[2:3], exec
	s_cselect_b32 s1, s31, s35
	s_cselect_b32 s29, s30, s34
	s_ashr_i32 s27, s26, 31
	s_lshl_b64 s[36:37], s[26:27], 20
	s_add_u32 s36, s33, s36
	s_addc_u32 s37, s48, s37
	s_and_b64 s[38:39], s[2:3], exec
	s_cselect_b32 s27, s37, s43
	s_cselect_b32 s41, s36, s42
	s_add_u32 s34, s34, 0x80080
	s_addc_u32 s35, s35, 0
	s_add_u32 s46, s42, 0x100
	v_mov_b32_e32 v98, 0
	s_addc_u32 s47, s43, 0
	s_mov_b32 s77, -2
	v_mov_b32_e32 v99, v98
	v_mov_b32_e32 v100, v98
	v_mov_b32_e32 v101, v98
	v_mov_b32_e32 v102, v98
	v_mov_b32_e32 v103, v98
	v_mov_b32_e32 v104, v98
	v_mov_b32_e32 v105, v98
	v_mov_b32_e32 v50, v98
	v_mov_b32_e32 v51, v98
	v_mov_b32_e32 v52, v98
	v_mov_b32_e32 v53, v98
	v_mov_b32_e32 v74, v98
	v_mov_b32_e32 v75, v98
	v_mov_b32_e32 v76, v98
	v_mov_b32_e32 v77, v98
	v_mov_b32_e32 v58, v98
	v_mov_b32_e32 v59, v98
	v_mov_b32_e32 v60, v98
	v_mov_b32_e32 v61, v98
	v_mov_b32_e32 v82, v98
	v_mov_b32_e32 v83, v98
	v_mov_b32_e32 v84, v98
	v_mov_b32_e32 v85, v98
	v_mov_b32_e32 v66, v98
	v_mov_b32_e32 v67, v98
	v_mov_b32_e32 v68, v98
	v_mov_b32_e32 v69, v98
	v_mov_b32_e32 v90, v98
	v_mov_b32_e32 v91, v98
	v_mov_b32_e32 v92, v98
	v_mov_b32_e32 v93, v98
	v_mov_b32_e32 v106, v98
	v_mov_b32_e32 v107, v98
	v_mov_b32_e32 v108, v98
	v_mov_b32_e32 v109, v98
	v_mov_b32_e32 v110, v98
	v_mov_b32_e32 v111, v98
	v_mov_b32_e32 v112, v98
	v_mov_b32_e32 v113, v98
	v_mov_b32_e32 v54, v98
	v_mov_b32_e32 v55, v98
	v_mov_b32_e32 v56, v98
	v_mov_b32_e32 v57, v98
	v_mov_b32_e32 v78, v98
	v_mov_b32_e32 v79, v98
	v_mov_b32_e32 v80, v98
	v_mov_b32_e32 v81, v98
	v_mov_b32_e32 v62, v98
	v_mov_b32_e32 v63, v98
	v_mov_b32_e32 v64, v98
	v_mov_b32_e32 v65, v98
	v_mov_b32_e32 v86, v98
	v_mov_b32_e32 v87, v98
	v_mov_b32_e32 v88, v98
	v_mov_b32_e32 v89, v98
	v_mov_b32_e32 v70, v98
	v_mov_b32_e32 v71, v98
	v_mov_b32_e32 v72, v98
	v_mov_b32_e32 v73, v98
	v_mov_b32_e32 v94, v98
	v_mov_b32_e32 v95, v98
	v_mov_b32_e32 v96, v98
	v_mov_b32_e32 v97, v98
	v_mov_b32_e32 v114, v98
	v_mov_b32_e32 v115, v98
	v_mov_b32_e32 v116, v98
	v_mov_b32_e32 v117, v98
	v_mov_b32_e32 v118, v98
	v_mov_b32_e32 v119, v98
	v_mov_b32_e32 v120, v98
	v_mov_b32_e32 v121, v98
	v_mov_b32_e32 v2, v98
	v_mov_b32_e32 v3, v98
	v_mov_b32_e32 v4, v98
	v_mov_b32_e32 v5, v98
	v_mov_b32_e32 v14, v98
	v_mov_b32_e32 v15, v98
	v_mov_b32_e32 v16, v98
	v_mov_b32_e32 v17, v98
	v_mov_b32_e32 v6, v98
	v_mov_b32_e32 v7, v98
	v_mov_b32_e32 v8, v98
	v_mov_b32_e32 v9, v98
	v_mov_b32_e32 v18, v98
	v_mov_b32_e32 v19, v98
	v_mov_b32_e32 v20, v98
	v_mov_b32_e32 v21, v98
	v_mov_b32_e32 v10, v98
	v_mov_b32_e32 v11, v98
	v_mov_b32_e32 v12, v98
	v_mov_b32_e32 v13, v98
	v_mov_b32_e32 v22, v98
	v_mov_b32_e32 v23, v98
	v_mov_b32_e32 v24, v98
	v_mov_b32_e32 v25, v98
	v_mov_b32_e32 v122, v98
	v_mov_b32_e32 v123, v98
	v_mov_b32_e32 v124, v98
	v_mov_b32_e32 v125, v98
	v_mov_b32_e32 v126, v98
	v_mov_b32_e32 v127, v98
	v_mov_b32_e32 v128, v98
	v_mov_b32_e32 v129, v98
	v_mov_b32_e32 v26, v98
	v_mov_b32_e32 v27, v98
	v_mov_b32_e32 v28, v98
	v_mov_b32_e32 v29, v98
	v_mov_b32_e32 v38, v98
	v_mov_b32_e32 v39, v98
	v_mov_b32_e32 v40, v98
	v_mov_b32_e32 v41, v98
	v_mov_b32_e32 v30, v98
	v_mov_b32_e32 v31, v98
	v_mov_b32_e32 v32, v98
	v_mov_b32_e32 v33, v98
	v_mov_b32_e32 v42, v98
	v_mov_b32_e32 v43, v98
	v_mov_b32_e32 v44, v98
	v_mov_b32_e32 v45, v98
	v_mov_b32_e32 v34, v98
	v_mov_b32_e32 v35, v98
	v_mov_b32_e32 v36, v98
	v_mov_b32_e32 v37, v98
	v_mov_b32_e32 v46, v98
	v_mov_b32_e32 v47, v98
	v_mov_b32_e32 v48, v98
	v_mov_b32_e32 v49, v98
	v_readfirstlane_b32 s38, v0
	s_nop 3
	s_lshr_b32 s38, s38, 6
	s_cmp_ge_u32 s38, 4
	s_cbranch_scc0 .Lprio_P8
	s_setprio 1
.Lprio_P8:
.LBB0_1649:
	ds_read_b128 v[130:133], v167
	ds_read_b128 v[134:137], v167 offset:1024
	ds_read_b128 v[138:141], v167 offset:2048
	ds_read_b128 v[142:145], v167 offset:3072
	ds_read_b128 v[168:171], v228
	ds_read_b128 v[172:175], v228 offset:1024
	ds_read_b128 v[176:179], v228 offset:2048
	ds_read_b128 v[180:183], v228 offset:3072
	s_add_u32 s38, s34, 0xfff80080
	s_addc_u32 s39, s35, -1
	s_cmp_eq_u32 s77, 28
	s_cselect_b32 s45, s1, s39
	s_cselect_b32 s44, s29, s38
	s_cselect_b32 s43, s27, s47
	s_cselect_b32 s42, s41, s46
	s_add_i32 m0, s50, 0xc000
	ds_read_b128 v[184:187], v229
	ds_read_b128 v[188:191], v229 offset:1024
	ds_read_b128 v[192:195], v229 offset:2048
	ds_read_b128 v[196:199], v229 offset:3072
	ds_read_b128 v[200:203], v229 offset:4096
	ds_read_b128 v[204:207], v229 offset:5120
	ds_read_b128 v[208:211], v229 offset:6144
	ds_read_b128 v[212:215], v229 offset:7168
	global_load_lds_dwordx4 v158, s[34:35]
	s_add_i32 m0, s50, 0xe000
	s_nop 0
	global_load_lds_dwordx4 v160, s[34:35]
	s_waitcnt vmcnt(8)
	s_waitcnt lgkmcnt(0)
	s_barrier
	s_waitcnt lgkmcnt(0)
	v_mfma_i32_16x16x64_i8 v[46:49], v[130:133], v[184:187], v[46:49]
	v_mfma_i32_16x16x64_i8 v[34:37], v[138:141], v[184:187], v[34:37]
	v_mfma_i32_16x16x64_i8 v[42:45], v[130:133], v[192:195], v[42:45]
	v_mfma_i32_16x16x64_i8 v[30:33], v[138:141], v[192:195], v[30:33]
	v_mfma_i32_16x16x64_i8 v[38:41], v[130:133], v[200:203], v[38:41]
	v_mfma_i32_16x16x64_i8 v[26:29], v[138:141], v[200:203], v[26:29]
	v_mfma_i32_16x16x64_i8 v[126:129], v[130:133], v[208:211], v[126:129]
	v_mfma_i32_16x16x64_i8 v[122:125], v[138:141], v[208:211], v[122:125]
	v_mfma_i32_16x16x64_i8 v[46:49], v[134:137], v[188:191], v[46:49]
	v_mfma_i32_16x16x64_i8 v[34:37], v[142:145], v[188:191], v[34:37]
	v_mfma_i32_16x16x64_i8 v[42:45], v[134:137], v[196:199], v[42:45]
	v_mfma_i32_16x16x64_i8 v[30:33], v[142:145], v[196:199], v[30:33]
	v_mfma_i32_16x16x64_i8 v[38:41], v[134:137], v[204:207], v[38:41]
	v_mfma_i32_16x16x64_i8 v[26:29], v[142:145], v[204:207], v[26:29]
	v_mfma_i32_16x16x64_i8 v[126:129], v[134:137], v[212:215], v[126:129]
	v_mfma_i32_16x16x64_i8 v[122:125], v[142:145], v[212:215], v[122:125]
	v_mfma_i32_16x16x64_i8 v[22:25], v[168:171], v[184:187], v[22:25]
	v_mfma_i32_16x16x64_i8 v[10:13], v[176:179], v[184:187], v[10:13]
	v_mfma_i32_16x16x64_i8 v[18:21], v[168:171], v[192:195], v[18:21]
	v_mfma_i32_16x16x64_i8 v[6:9], v[176:179], v[192:195], v[6:9]
	v_mfma_i32_16x16x64_i8 v[14:17], v[168:171], v[200:203], v[14:17]
	v_mfma_i32_16x16x64_i8 v[2:5], v[176:179], v[200:203], v[2:5]
	v_mfma_i32_16x16x64_i8 v[118:121], v[168:171], v[208:211], v[118:121]
	v_mfma_i32_16x16x64_i8 v[114:117], v[176:179], v[208:211], v[114:117]
	v_mfma_i32_16x16x64_i8 v[22:25], v[172:175], v[188:191], v[22:25]
	v_mfma_i32_16x16x64_i8 v[10:13], v[180:183], v[188:191], v[10:13]
	v_mfma_i32_16x16x64_i8 v[18:21], v[172:175], v[196:199], v[18:21]
	v_mfma_i32_16x16x64_i8 v[6:9], v[180:183], v[196:199], v[6:9]
	v_mfma_i32_16x16x64_i8 v[14:17], v[172:175], v[204:207], v[14:17]
	v_mfma_i32_16x16x64_i8 v[2:5], v[180:183], v[204:207], v[2:5]
	v_mfma_i32_16x16x64_i8 v[118:121], v[172:175], v[212:215], v[118:121]
	v_mfma_i32_16x16x64_i8 v[114:117], v[180:183], v[212:215], v[114:117]
	s_barrier
	s_add_u32 s98, s42, s14
	s_addc_u32 s99, s43, s15
	s_add_u32 s100, s44, s14
	s_addc_u32 s101, s45, s15
	s_add_i32 s38, s64, s49
	s_mov_b32 m0, s38
	ds_read_b128 v[184:187], v229 offset:16384
	ds_read_b128 v[188:191], v229 offset:17408
	ds_read_b128 v[192:195], v229 offset:18432
	ds_read_b128 v[196:199], v229 offset:19456
	ds_read_b128 v[200:203], v229 offset:20480
	ds_read_b128 v[204:207], v229 offset:21504
	ds_read_b128 v[208:211], v229 offset:22528
	ds_read_b128 v[212:215], v229 offset:23552
	global_load_lds_dwordx4 v150, s[42:43]
	s_add_i32 m0, s38, 0x2000
	s_add_u32 s38, s42, 0x80000
	s_addc_u32 s39, s43, 0
	s_add_i32 s78, s65, s49
	global_load_lds_dwordx4 v154, s[42:43]
	s_mov_b32 m0, s78
	s_nop 0
	global_load_lds_dwordx4 v150, s[38:39]
	s_add_i32 m0, s78, 0x2000
	s_nop 0
	global_load_lds_dwordx4 v154, s[38:39]
	s_mov_b32 m0, s50
	s_nop 0
	global_load_lds_dwordx4 v148, s[44:45]
	s_mov_b32 m0, s51
	s_nop 0
	global_load_lds_dwordx4 v152, s[44:45]
	s_waitcnt vmcnt(8)
	s_waitcnt lgkmcnt(0)
	s_barrier
	s_waitcnt lgkmcnt(0)
	v_mfma_i32_16x16x64_i8 v[94:97], v[130:133], v[184:187], v[94:97]
	v_mfma_i32_16x16x64_i8 v[70:73], v[138:141], v[184:187], v[70:73]
	v_mfma_i32_16x16x64_i8 v[86:89], v[130:133], v[192:195], v[86:89]
	v_mfma_i32_16x16x64_i8 v[62:65], v[138:141], v[192:195], v[62:65]
	v_mfma_i32_16x16x64_i8 v[78:81], v[130:133], v[200:203], v[78:81]
	v_mfma_i32_16x16x64_i8 v[54:57], v[138:141], v[200:203], v[54:57]
	v_mfma_i32_16x16x64_i8 v[110:113], v[130:133], v[208:211], v[110:113]
	v_mfma_i32_16x16x64_i8 v[106:109], v[138:141], v[208:211], v[106:109]
	v_mfma_i32_16x16x64_i8 v[94:97], v[134:137], v[188:191], v[94:97]
	v_mfma_i32_16x16x64_i8 v[70:73], v[142:145], v[188:191], v[70:73]
	v_mfma_i32_16x16x64_i8 v[86:89], v[134:137], v[196:199], v[86:89]
	v_mfma_i32_16x16x64_i8 v[62:65], v[142:145], v[196:199], v[62:65]
	v_mfma_i32_16x16x64_i8 v[78:81], v[134:137], v[204:207], v[78:81]
	v_mfma_i32_16x16x64_i8 v[54:57], v[142:145], v[204:207], v[54:57]
	v_mfma_i32_16x16x64_i8 v[110:113], v[134:137], v[212:215], v[110:113]
	v_mfma_i32_16x16x64_i8 v[106:109], v[142:145], v[212:215], v[106:109]
	v_mfma_i32_16x16x64_i8 v[90:93], v[168:171], v[184:187], v[90:93]
	v_mfma_i32_16x16x64_i8 v[66:69], v[176:179], v[184:187], v[66:69]
	v_mfma_i32_16x16x64_i8 v[82:85], v[168:171], v[192:195], v[82:85]
	v_mfma_i32_16x16x64_i8 v[58:61], v[176:179], v[192:195], v[58:61]
	v_mfma_i32_16x16x64_i8 v[74:77], v[168:171], v[200:203], v[74:77]
	v_mfma_i32_16x16x64_i8 v[50:53], v[176:179], v[200:203], v[50:53]
	v_mfma_i32_16x16x64_i8 v[102:105], v[168:171], v[208:211], v[102:105]
	v_mfma_i32_16x16x64_i8 v[98:101], v[176:179], v[208:211], v[98:101]
	v_mfma_i32_16x16x64_i8 v[90:93], v[172:175], v[188:191], v[90:93]
	v_mfma_i32_16x16x64_i8 v[66:69], v[180:183], v[188:191], v[66:69]
	v_mfma_i32_16x16x64_i8 v[82:85], v[172:175], v[196:199], v[82:85]
	v_mfma_i32_16x16x64_i8 v[58:61], v[180:183], v[196:199], v[58:61]
	v_mfma_i32_16x16x64_i8 v[74:77], v[172:175], v[204:207], v[74:77]
	v_mfma_i32_16x16x64_i8 v[50:53], v[180:183], v[204:207], v[50:53]
	v_mfma_i32_16x16x64_i8 v[102:105], v[172:175], v[212:215], v[102:105]
	v_mfma_i32_16x16x64_i8 v[98:101], v[180:183], v[212:215], v[98:101]
	s_barrier
	s_add_i32 s78, 0, 0x18000
	s_add_i32 s79, 0, 0x1c000
	v_add_u32_e32 v142, s78, v1
	v_add_u32_e32 v156, s79, v1
	ds_read_b128 v[130:133], v142
	ds_read_b128 v[134:137], v142 offset:1024
	ds_read_b128 v[138:141], v142 offset:2048
	ds_read_b128 v[142:145], v142 offset:3072
	ds_read_b128 v[168:171], v156
	ds_read_b128 v[172:175], v156 offset:1024
	ds_read_b128 v[176:179], v156 offset:2048
	ds_read_b128 v[180:183], v156 offset:3072
	s_add_u32 s38, s44, 0x80000
	s_addc_u32 s39, s45, 0
	s_mov_b32 m0, s52
	ds_read_b128 v[184:187], v229 offset:32768
	ds_read_b128 v[188:191], v229 offset:33792
	ds_read_b128 v[192:195], v229 offset:34816
	ds_read_b128 v[196:199], v229 offset:35840
	ds_read_b128 v[200:203], v229 offset:36864
	ds_read_b128 v[204:207], v229 offset:37888
	ds_read_b128 v[208:211], v229 offset:38912
	ds_read_b128 v[212:215], v229 offset:39936
	global_load_lds_dwordx4 v148, s[38:39]
	s_mov_b32 m0, s53
	s_nop 0
	global_load_lds_dwordx4 v152, s[38:39]
	s_waitcnt vmcnt(8)
	s_waitcnt lgkmcnt(0)
	s_barrier
	s_waitcnt lgkmcnt(0)
	v_mfma_i32_16x16x64_i8 v[46:49], v[130:133], v[184:187], v[46:49]
	v_mfma_i32_16x16x64_i8 v[34:37], v[138:141], v[184:187], v[34:37]
	v_mfma_i32_16x16x64_i8 v[42:45], v[130:133], v[192:195], v[42:45]
	v_mfma_i32_16x16x64_i8 v[30:33], v[138:141], v[192:195], v[30:33]
	v_mfma_i32_16x16x64_i8 v[38:41], v[130:133], v[200:203], v[38:41]
	v_mfma_i32_16x16x64_i8 v[26:29], v[138:141], v[200:203], v[26:29]
	v_mfma_i32_16x16x64_i8 v[126:129], v[130:133], v[208:211], v[126:129]
	v_mfma_i32_16x16x64_i8 v[122:125], v[138:141], v[208:211], v[122:125]
	v_mfma_i32_16x16x64_i8 v[46:49], v[134:137], v[188:191], v[46:49]
	v_mfma_i32_16x16x64_i8 v[34:37], v[142:145], v[188:191], v[34:37]
	v_mfma_i32_16x16x64_i8 v[42:45], v[134:137], v[196:199], v[42:45]
	v_mfma_i32_16x16x64_i8 v[30:33], v[142:145], v[196:199], v[30:33]
	v_mfma_i32_16x16x64_i8 v[38:41], v[134:137], v[204:207], v[38:41]
	v_mfma_i32_16x16x64_i8 v[26:29], v[142:145], v[204:207], v[26:29]
	v_mfma_i32_16x16x64_i8 v[126:129], v[134:137], v[212:215], v[126:129]
	v_mfma_i32_16x16x64_i8 v[122:125], v[142:145], v[212:215], v[122:125]
	v_mfma_i32_16x16x64_i8 v[22:25], v[168:171], v[184:187], v[22:25]
	v_mfma_i32_16x16x64_i8 v[10:13], v[176:179], v[184:187], v[10:13]
	v_mfma_i32_16x16x64_i8 v[18:21], v[168:171], v[192:195], v[18:21]
	v_mfma_i32_16x16x64_i8 v[6:9], v[176:179], v[192:195], v[6:9]
	v_mfma_i32_16x16x64_i8 v[14:17], v[168:171], v[200:203], v[14:17]
	v_mfma_i32_16x16x64_i8 v[2:5], v[176:179], v[200:203], v[2:5]
	v_mfma_i32_16x16x64_i8 v[118:121], v[168:171], v[208:211], v[118:121]
	v_mfma_i32_16x16x64_i8 v[114:117], v[176:179], v[208:211], v[114:117]
	v_mfma_i32_16x16x64_i8 v[22:25], v[172:175], v[188:191], v[22:25]
	v_mfma_i32_16x16x64_i8 v[10:13], v[180:183], v[188:191], v[10:13]
	v_mfma_i32_16x16x64_i8 v[18:21], v[172:175], v[196:199], v[18:21]
	v_mfma_i32_16x16x64_i8 v[6:9], v[180:183], v[196:199], v[6:9]
	v_mfma_i32_16x16x64_i8 v[14:17], v[172:175], v[204:207], v[14:17]
	v_mfma_i32_16x16x64_i8 v[2:5], v[180:183], v[204:207], v[2:5]
	v_mfma_i32_16x16x64_i8 v[118:121], v[172:175], v[212:215], v[118:121]
	v_mfma_i32_16x16x64_i8 v[114:117], v[180:183], v[212:215], v[114:117]
	s_barrier
	s_add_i32 s38, s78, s49
	s_mov_b32 m0, s38
	ds_read_b128 v[184:187], v229 offset:49152
	ds_read_b128 v[188:191], v229 offset:50176
	ds_read_b128 v[192:195], v229 offset:51200
	ds_read_b128 v[196:199], v229 offset:52224
	ds_read_b128 v[200:203], v229 offset:53248
	ds_read_b128 v[204:207], v229 offset:54272
	ds_read_b128 v[208:211], v229 offset:55296
	ds_read_b128 v[212:215], v229 offset:56320
	global_load_lds_dwordx4 v150, s[98:99]
	s_add_i32 m0, s38, 0x2000
	s_add_u32 s38, s42, 0x80080
	s_addc_u32 s39, s43, 0
	s_add_i32 s42, s79, s49
	global_load_lds_dwordx4 v154, s[98:99]
	s_mov_b32 m0, s42
	s_nop 0
	global_load_lds_dwordx4 v150, s[38:39]
	s_add_i32 m0, s42, 0x2000
	s_nop 0
	global_load_lds_dwordx4 v154, s[38:39]
	s_mov_b32 m0, s57
	s_nop 0
	global_load_lds_dwordx4 v148, s[100:101]
	s_mov_b32 m0, s58
	s_nop 0
	global_load_lds_dwordx4 v152, s[100:101]
	s_waitcnt vmcnt(8)
	s_waitcnt lgkmcnt(0)
	s_barrier
	s_waitcnt lgkmcnt(0)
	v_mfma_i32_16x16x64_i8 v[94:97], v[130:133], v[184:187], v[94:97]
	v_mfma_i32_16x16x64_i8 v[70:73], v[138:141], v[184:187], v[70:73]
	v_mfma_i32_16x16x64_i8 v[86:89], v[130:133], v[192:195], v[86:89]
	v_mfma_i32_16x16x64_i8 v[62:65], v[138:141], v[192:195], v[62:65]
	v_mfma_i32_16x16x64_i8 v[78:81], v[130:133], v[200:203], v[78:81]
	v_mfma_i32_16x16x64_i8 v[54:57], v[138:141], v[200:203], v[54:57]
	v_mfma_i32_16x16x64_i8 v[110:113], v[130:133], v[208:211], v[110:113]
	v_mfma_i32_16x16x64_i8 v[106:109], v[138:141], v[208:211], v[106:109]
	v_mfma_i32_16x16x64_i8 v[94:97], v[134:137], v[188:191], v[94:97]
	v_mfma_i32_16x16x64_i8 v[70:73], v[142:145], v[188:191], v[70:73]
	v_mfma_i32_16x16x64_i8 v[86:89], v[134:137], v[196:199], v[86:89]
	v_mfma_i32_16x16x64_i8 v[62:65], v[142:145], v[196:199], v[62:65]
	v_mfma_i32_16x16x64_i8 v[78:81], v[134:137], v[204:207], v[78:81]
	v_mfma_i32_16x16x64_i8 v[54:57], v[142:145], v[204:207], v[54:57]
	v_mfma_i32_16x16x64_i8 v[110:113], v[134:137], v[212:215], v[110:113]
	v_mfma_i32_16x16x64_i8 v[106:109], v[142:145], v[212:215], v[106:109]
	v_mfma_i32_16x16x64_i8 v[90:93], v[168:171], v[184:187], v[90:93]
	v_mfma_i32_16x16x64_i8 v[66:69], v[176:179], v[184:187], v[66:69]
	v_mfma_i32_16x16x64_i8 v[82:85], v[168:171], v[192:195], v[82:85]
	v_mfma_i32_16x16x64_i8 v[58:61], v[176:179], v[192:195], v[58:61]
	v_mfma_i32_16x16x64_i8 v[74:77], v[168:171], v[200:203], v[74:77]
	v_mfma_i32_16x16x64_i8 v[50:53], v[176:179], v[200:203], v[50:53]
	v_mfma_i32_16x16x64_i8 v[102:105], v[168:171], v[208:211], v[102:105]
	v_mfma_i32_16x16x64_i8 v[98:101], v[176:179], v[208:211], v[98:101]
	v_mfma_i32_16x16x64_i8 v[90:93], v[172:175], v[188:191], v[90:93]
	v_mfma_i32_16x16x64_i8 v[66:69], v[180:183], v[188:191], v[66:69]
	v_mfma_i32_16x16x64_i8 v[82:85], v[172:175], v[196:199], v[82:85]
	v_mfma_i32_16x16x64_i8 v[58:61], v[180:183], v[196:199], v[58:61]
	v_mfma_i32_16x16x64_i8 v[74:77], v[172:175], v[204:207], v[74:77]
	v_mfma_i32_16x16x64_i8 v[50:53], v[180:183], v[204:207], v[50:53]
	v_mfma_i32_16x16x64_i8 v[102:105], v[172:175], v[212:215], v[102:105]
	v_mfma_i32_16x16x64_i8 v[98:101], v[180:183], v[212:215], v[98:101]
	s_barrier
	s_add_i32 s77, s77, 2
	s_add_u32 s34, s34, 0x100
	s_addc_u32 s35, s35, 0
	s_add_u32 s46, s46, 0x100
	s_addc_u32 s47, s47, 0
	s_cmp_gt_u32 s77, 29
	s_cbranch_scc0 .LBB0_1649
	s_setprio 0
	s_and_b64 vcc, exec, s[16:17]
	s_cbranch_vccz .LBB0_1652
	s_barrier

.LBB0_1898:
	s_add_u32 s20, s20, 0x158080
	s_addc_u32 s21, s21, 0
	s_add_u32 s47, s22, 0x100
	v_mov_b32_e32 v2, 0
	s_addc_u32 s48, s23, 0
	s_mov_b32 s49, -2
	v_mov_b32_e32 v3, v2
	v_mov_b32_e32 v4, v2
	v_mov_b32_e32 v5, v2
	v_mov_b32_e32 v6, v2
	v_mov_b32_e32 v7, v2
	v_mov_b32_e32 v8, v2
	v_mov_b32_e32 v9, v2
	v_mov_b32_e32 v18, v2
	v_mov_b32_e32 v19, v2
	v_mov_b32_e32 v20, v2
	v_mov_b32_e32 v21, v2
	v_mov_b32_e32 v22, v2
	v_mov_b32_e32 v23, v2
	v_mov_b32_e32 v24, v2
	v_mov_b32_e32 v25, v2
	v_mov_b32_e32 v34, v2
	v_mov_b32_e32 v35, v2
	v_mov_b32_e32 v36, v2
	v_mov_b32_e32 v37, v2
	v_mov_b32_e32 v38, v2
	v_mov_b32_e32 v39, v2
	v_mov_b32_e32 v40, v2
	v_mov_b32_e32 v41, v2
	v_mov_b32_e32 v50, v2
	v_mov_b32_e32 v51, v2
	v_mov_b32_e32 v52, v2
	v_mov_b32_e32 v53, v2
	v_mov_b32_e32 v54, v2
	v_mov_b32_e32 v55, v2
	v_mov_b32_e32 v56, v2
	v_mov_b32_e32 v57, v2
	v_mov_b32_e32 v10, v2
	v_mov_b32_e32 v11, v2
	v_mov_b32_e32 v12, v2
	v_mov_b32_e32 v13, v2
	v_mov_b32_e32 v14, v2
	v_mov_b32_e32 v15, v2
	v_mov_b32_e32 v16, v2
	v_mov_b32_e32 v17, v2
	v_mov_b32_e32 v26, v2
	v_mov_b32_e32 v27, v2
	v_mov_b32_e32 v28, v2
	v_mov_b32_e32 v29, v2
	v_mov_b32_e32 v30, v2
	v_mov_b32_e32 v31, v2
	v_mov_b32_e32 v32, v2
	v_mov_b32_e32 v33, v2
	v_mov_b32_e32 v42, v2
	v_mov_b32_e32 v43, v2
	v_mov_b32_e32 v44, v2
	v_mov_b32_e32 v45, v2
	v_mov_b32_e32 v46, v2
	v_mov_b32_e32 v47, v2
	v_mov_b32_e32 v48, v2
	v_mov_b32_e32 v49, v2
	v_mov_b32_e32 v58, v2
	v_mov_b32_e32 v59, v2
	v_mov_b32_e32 v60, v2
	v_mov_b32_e32 v61, v2
	v_mov_b32_e32 v62, v2
	v_mov_b32_e32 v63, v2
	v_mov_b32_e32 v64, v2
	v_mov_b32_e32 v65, v2
	v_mov_b32_e32 v66, v2
	v_mov_b32_e32 v67, v2
	v_mov_b32_e32 v68, v2
	v_mov_b32_e32 v69, v2
	v_mov_b32_e32 v70, v2
	v_mov_b32_e32 v71, v2
	v_mov_b32_e32 v72, v2
	v_mov_b32_e32 v73, v2
	v_mov_b32_e32 v82, v2
	v_mov_b32_e32 v83, v2
	v_mov_b32_e32 v84, v2
	v_mov_b32_e32 v85, v2
	v_mov_b32_e32 v86, v2
	v_mov_b32_e32 v87, v2
	v_mov_b32_e32 v88, v2
	v_mov_b32_e32 v89, v2
	v_mov_b32_e32 v98, v2
	v_mov_b32_e32 v99, v2
	v_mov_b32_e32 v100, v2
	v_mov_b32_e32 v101, v2
	v_mov_b32_e32 v102, v2
	v_mov_b32_e32 v103, v2
	v_mov_b32_e32 v104, v2
	v_mov_b32_e32 v105, v2
	v_mov_b32_e32 v114, v2
	v_mov_b32_e32 v115, v2
	v_mov_b32_e32 v116, v2
	v_mov_b32_e32 v117, v2
	v_mov_b32_e32 v118, v2
	v_mov_b32_e32 v119, v2
	v_mov_b32_e32 v120, v2
	v_mov_b32_e32 v121, v2
	v_mov_b32_e32 v74, v2
	v_mov_b32_e32 v75, v2
	v_mov_b32_e32 v76, v2
	v_mov_b32_e32 v77, v2
	v_mov_b32_e32 v78, v2
	v_mov_b32_e32 v79, v2
	v_mov_b32_e32 v80, v2
	v_mov_b32_e32 v81, v2
	v_mov_b32_e32 v90, v2
	v_mov_b32_e32 v91, v2
	v_mov_b32_e32 v92, v2
	v_mov_b32_e32 v93, v2
	v_mov_b32_e32 v94, v2
	v_mov_b32_e32 v95, v2
	v_mov_b32_e32 v96, v2
	v_mov_b32_e32 v97, v2
	v_mov_b32_e32 v106, v2
	v_mov_b32_e32 v107, v2
	v_mov_b32_e32 v108, v2
	v_mov_b32_e32 v109, v2
	v_mov_b32_e32 v110, v2
	v_mov_b32_e32 v111, v2
	v_mov_b32_e32 v112, v2
	v_mov_b32_e32 v113, v2
	v_mov_b32_e32 v138, v2
	v_mov_b32_e32 v139, v2
	v_mov_b32_e32 v140, v2
	v_mov_b32_e32 v141, v2
	v_mov_b32_e32 v142, v2
	v_mov_b32_e32 v143, v2
	v_mov_b32_e32 v144, v2
	v_mov_b32_e32 v145, v2
	v_readfirstlane_b32 s22, v0
	s_nop 3
	s_lshr_b32 s22, s22, 6
	s_cmp_ge_u32 s22, 4
	s_cbranch_scc0 .Lprio_P10
	s_setprio 1
.Lprio_P10:
.LBB0_1899:
	ds_read_b128 v[122:125], v169
	ds_read_b128 v[126:129], v169 offset:1024
	ds_read_b128 v[130:133], v169 offset:2048
	ds_read_b128 v[134:137], v169 offset:3072
	ds_read_b128 v[172:175], v170
	ds_read_b128 v[176:179], v170 offset:1024
	ds_read_b128 v[180:183], v170 offset:2048
	ds_read_b128 v[184:187], v170 offset:3072
	s_add_u32 s22, s20, 0xffea8080
	s_addc_u32 s23, s21, -1
	s_cmpk_eq_i32 s49, 0x52
	s_cselect_b32 s25, s5, s23
	s_cselect_b32 s24, s4, s22
	s_cselect_b32 s23, s19, s48
	s_cselect_b32 s22, s18, s47
	s_add_i32 m0, s30, 0xc000
	ds_read_b128 v[188:191], v171
	ds_read_b128 v[192:195], v171 offset:1024
	ds_read_b128 v[196:199], v171 offset:2048
	ds_read_b128 v[200:203], v171 offset:3072
	ds_read_b128 v[204:207], v171 offset:4096
	ds_read_b128 v[208:211], v171 offset:5120
	ds_read_b128 v[212:215], v171 offset:6144
	ds_read_b128 v[216:219], v171 offset:7168
	global_load_lds_dwordx4 v156, s[20:21]
	s_add_i32 m0, s30, 0xe000
	s_nop 0
	global_load_lds_dwordx4 v158, s[20:21]
	s_waitcnt vmcnt(8)
	s_waitcnt lgkmcnt(0)
	s_barrier
	s_waitcnt lgkmcnt(0)
	v_mfma_i32_16x16x64_i8 v[142:145], v[122:125], v[188:191], v[142:145]
	v_mfma_i32_16x16x64_i8 v[138:141], v[130:133], v[188:191], v[138:141]
	v_mfma_i32_16x16x64_i8 v[110:113], v[122:125], v[196:199], v[110:113]
	v_mfma_i32_16x16x64_i8 v[106:109], v[130:133], v[196:199], v[106:109]
	v_mfma_i32_16x16x64_i8 v[94:97], v[122:125], v[204:207], v[94:97]
	v_mfma_i32_16x16x64_i8 v[90:93], v[130:133], v[204:207], v[90:93]
	v_mfma_i32_16x16x64_i8 v[78:81], v[122:125], v[212:215], v[78:81]
	v_mfma_i32_16x16x64_i8 v[74:77], v[130:133], v[212:215], v[74:77]
	v_mfma_i32_16x16x64_i8 v[142:145], v[126:129], v[192:195], v[142:145]
	v_mfma_i32_16x16x64_i8 v[138:141], v[134:137], v[192:195], v[138:141]
	v_mfma_i32_16x16x64_i8 v[110:113], v[126:129], v[200:203], v[110:113]
	v_mfma_i32_16x16x64_i8 v[106:109], v[134:137], v[200:203], v[106:109]
	v_mfma_i32_16x16x64_i8 v[94:97], v[126:129], v[208:211], v[94:97]
	v_mfma_i32_16x16x64_i8 v[90:93], v[134:137], v[208:211], v[90:93]
	v_mfma_i32_16x16x64_i8 v[78:81], v[126:129], v[216:219], v[78:81]
	v_mfma_i32_16x16x64_i8 v[74:77], v[134:137], v[216:219], v[74:77]
	v_mfma_i32_16x16x64_i8 v[118:121], v[172:175], v[188:191], v[118:121]
	v_mfma_i32_16x16x64_i8 v[114:117], v[180:183], v[188:191], v[114:117]
	v_mfma_i32_16x16x64_i8 v[102:105], v[172:175], v[196:199], v[102:105]
	v_mfma_i32_16x16x64_i8 v[98:101], v[180:183], v[196:199], v[98:101]
	v_mfma_i32_16x16x64_i8 v[86:89], v[172:175], v[204:207], v[86:89]
	v_mfma_i32_16x16x64_i8 v[82:85], v[180:183], v[204:207], v[82:85]
	v_mfma_i32_16x16x64_i8 v[70:73], v[172:175], v[212:215], v[70:73]
	v_mfma_i32_16x16x64_i8 v[66:69], v[180:183], v[212:215], v[66:69]
	v_mfma_i32_16x16x64_i8 v[118:121], v[176:179], v[192:195], v[118:121]
	v_mfma_i32_16x16x64_i8 v[114:117], v[184:187], v[192:195], v[114:117]
	v_mfma_i32_16x16x64_i8 v[102:105], v[176:179], v[200:203], v[102:105]
	v_mfma_i32_16x16x64_i8 v[98:101], v[184:187], v[200:203], v[98:101]
	v_mfma_i32_16x16x64_i8 v[86:89], v[176:179], v[208:211], v[86:89]
	v_mfma_i32_16x16x64_i8 v[82:85], v[184:187], v[208:211], v[82:85]
	v_mfma_i32_16x16x64_i8 v[70:73], v[176:179], v[216:219], v[70:73]
	v_mfma_i32_16x16x64_i8 v[66:69], v[184:187], v[216:219], v[66:69]
	s_barrier
	s_add_u32 s98, s22, s14
	s_addc_u32 s99, s23, s15
	s_add_u32 s100, s24, s14
	s_addc_u32 s101, s25, s15
	s_add_i32 s38, s41, s29
	s_mov_b32 m0, s38
	ds_read_b128 v[188:191], v171 offset:16384
	ds_read_b128 v[192:195], v171 offset:17408
	ds_read_b128 v[196:199], v171 offset:18432
	ds_read_b128 v[200:203], v171 offset:19456
	ds_read_b128 v[204:207], v171 offset:20480
	ds_read_b128 v[208:211], v171 offset:21504
	ds_read_b128 v[212:215], v171 offset:22528
	ds_read_b128 v[216:219], v171 offset:23552
	global_load_lds_dwordx4 v148, s[22:23]
	s_add_i32 m0, s38, 0x2000
	s_add_u32 s38, s22, 0x158000
	s_addc_u32 s39, s23, 0
	s_add_i32 s50, s42, s29
	global_load_lds_dwordx4 v152, s[22:23]
	s_mov_b32 m0, s50
	s_nop 0
	global_load_lds_dwordx4 v148, s[38:39]
	s_add_i32 m0, s50, 0x2000
	s_nop 0
	global_load_lds_dwordx4 v152, s[38:39]
	s_mov_b32 m0, s30
	s_nop 0
	global_load_lds_dwordx4 v146, s[24:25]
	s_mov_b32 m0, s31
	s_nop 0
	global_load_lds_dwordx4 v150, s[24:25]
	s_waitcnt vmcnt(8)
	s_waitcnt lgkmcnt(0)
	s_barrier
	s_waitcnt lgkmcnt(0)
	v_mfma_i32_16x16x64_i8 v[62:65], v[122:125], v[188:191], v[62:65]
	v_mfma_i32_16x16x64_i8 v[58:61], v[130:133], v[188:191], v[58:61]
	v_mfma_i32_16x16x64_i8 v[46:49], v[122:125], v[196:199], v[46:49]
	v_mfma_i32_16x16x64_i8 v[42:45], v[130:133], v[196:199], v[42:45]
	v_mfma_i32_16x16x64_i8 v[30:33], v[122:125], v[204:207], v[30:33]
	v_mfma_i32_16x16x64_i8 v[26:29], v[130:133], v[204:207], v[26:29]
	v_mfma_i32_16x16x64_i8 v[14:17], v[122:125], v[212:215], v[14:17]
	v_mfma_i32_16x16x64_i8 v[10:13], v[130:133], v[212:215], v[10:13]
	v_mfma_i32_16x16x64_i8 v[62:65], v[126:129], v[192:195], v[62:65]
	v_mfma_i32_16x16x64_i8 v[58:61], v[134:137], v[192:195], v[58:61]
	v_mfma_i32_16x16x64_i8 v[46:49], v[126:129], v[200:203], v[46:49]
	v_mfma_i32_16x16x64_i8 v[42:45], v[134:137], v[200:203], v[42:45]
	v_mfma_i32_16x16x64_i8 v[30:33], v[126:129], v[208:211], v[30:33]
	v_mfma_i32_16x16x64_i8 v[26:29], v[134:137], v[208:211], v[26:29]
	v_mfma_i32_16x16x64_i8 v[14:17], v[126:129], v[216:219], v[14:17]
	v_mfma_i32_16x16x64_i8 v[10:13], v[134:137], v[216:219], v[10:13]
	v_mfma_i32_16x16x64_i8 v[54:57], v[172:175], v[188:191], v[54:57]
	v_mfma_i32_16x16x64_i8 v[50:53], v[180:183], v[188:191], v[50:53]
	v_mfma_i32_16x16x64_i8 v[38:41], v[172:175], v[196:199], v[38:41]
	v_mfma_i32_16x16x64_i8 v[34:37], v[180:183], v[196:199], v[34:37]
	v_mfma_i32_16x16x64_i8 v[22:25], v[172:175], v[204:207], v[22:25]
	v_mfma_i32_16x16x64_i8 v[18:21], v[180:183], v[204:207], v[18:21]
	v_mfma_i32_16x16x64_i8 v[6:9], v[172:175], v[212:215], v[6:9]
	v_mfma_i32_16x16x64_i8 v[2:5], v[180:183], v[212:215], v[2:5]
	v_mfma_i32_16x16x64_i8 v[54:57], v[176:179], v[192:195], v[54:57]
	v_mfma_i32_16x16x64_i8 v[50:53], v[184:187], v[192:195], v[50:53]
	v_mfma_i32_16x16x64_i8 v[38:41], v[176:179], v[200:203], v[38:41]
	v_mfma_i32_16x16x64_i8 v[34:37], v[184:187], v[200:203], v[34:37]
	v_mfma_i32_16x16x64_i8 v[22:25], v[176:179], v[208:211], v[22:25]
	v_mfma_i32_16x16x64_i8 v[18:21], v[184:187], v[208:211], v[18:21]
	v_mfma_i32_16x16x64_i8 v[6:9], v[176:179], v[216:219], v[6:9]
	v_mfma_i32_16x16x64_i8 v[2:5], v[184:187], v[216:219], v[2:5]
	s_barrier
	s_add_i32 s38, 0, 0x18000
	s_add_i32 s39, 0, 0x1c000
	v_add_u32_e32 v134, s38, v167
	v_add_u32_e32 v154, s39, v167
	ds_read_b128 v[122:125], v134
	ds_read_b128 v[126:129], v134 offset:1024
	ds_read_b128 v[130:133], v134 offset:2048
	ds_read_b128 v[134:137], v134 offset:3072
	ds_read_b128 v[172:175], v154
	ds_read_b128 v[176:179], v154 offset:1024
	ds_read_b128 v[180:183], v154 offset:2048
	ds_read_b128 v[184:187], v154 offset:3072
	s_add_u32 s24, s24, 0x158000
	s_addc_u32 s25, s25, 0
	s_mov_b32 m0, s33
	ds_read_b128 v[188:191], v171 offset:32768
	ds_read_b128 v[192:195], v171 offset:33792
	ds_read_b128 v[196:199], v171 offset:34816
	ds_read_b128 v[200:203], v171 offset:35840
	ds_read_b128 v[204:207], v171 offset:36864
	ds_read_b128 v[208:211], v171 offset:37888
	ds_read_b128 v[212:215], v171 offset:38912
	ds_read_b128 v[216:219], v171 offset:39936
	global_load_lds_dwordx4 v146, s[24:25]
	s_mov_b32 m0, s34
	s_nop 0
	global_load_lds_dwordx4 v150, s[24:25]
	s_waitcnt vmcnt(8)
	s_waitcnt lgkmcnt(0)
	s_barrier
	s_waitcnt lgkmcnt(0)
	v_mfma_i32_16x16x64_i8 v[142:145], v[122:125], v[188:191], v[142:145]
	v_mfma_i32_16x16x64_i8 v[138:141], v[130:133], v[188:191], v[138:141]
	v_mfma_i32_16x16x64_i8 v[110:113], v[122:125], v[196:199], v[110:113]
	v_mfma_i32_16x16x64_i8 v[106:109], v[130:133], v[196:199], v[106:109]
	v_mfma_i32_16x16x64_i8 v[94:97], v[122:125], v[204:207], v[94:97]
	v_mfma_i32_16x16x64_i8 v[90:93], v[130:133], v[204:207], v[90:93]
	v_mfma_i32_16x16x64_i8 v[78:81], v[122:125], v[212:215], v[78:81]
	v_mfma_i32_16x16x64_i8 v[74:77], v[130:133], v[212:215], v[74:77]
	v_mfma_i32_16x16x64_i8 v[142:145], v[126:129], v[192:195], v[142:145]
	v_mfma_i32_16x16x64_i8 v[138:141], v[134:137], v[192:195], v[138:141]
	v_mfma_i32_16x16x64_i8 v[110:113], v[126:129], v[200:203], v[110:113]
	v_mfma_i32_16x16x64_i8 v[106:109], v[134:137], v[200:203], v[106:109]
	v_mfma_i32_16x16x64_i8 v[94:97], v[126:129], v[208:211], v[94:97]
	v_mfma_i32_16x16x64_i8 v[90:93], v[134:137], v[208:211], v[90:93]
	v_mfma_i32_16x16x64_i8 v[78:81], v[126:129], v[216:219], v[78:81]
	v_mfma_i32_16x16x64_i8 v[74:77], v[134:137], v[216:219], v[74:77]
	v_mfma_i32_16x16x64_i8 v[118:121], v[172:175], v[188:191], v[118:121]
	v_mfma_i32_16x16x64_i8 v[114:117], v[180:183], v[188:191], v[114:117]
	v_mfma_i32_16x16x64_i8 v[102:105], v[172:175], v[196:199], v[102:105]
	v_mfma_i32_16x16x64_i8 v[98:101], v[180:183], v[196:199], v[98:101]
	v_mfma_i32_16x16x64_i8 v[86:89], v[172:175], v[204:207], v[86:89]
	v_mfma_i32_16x16x64_i8 v[82:85], v[180:183], v[204:207], v[82:85]
	v_mfma_i32_16x16x64_i8 v[70:73], v[172:175], v[212:215], v[70:73]
	v_mfma_i32_16x16x64_i8 v[66:69], v[180:183], v[212:215], v[66:69]
	v_mfma_i32_16x16x64_i8 v[118:121], v[176:179], v[192:195], v[118:121]
	v_mfma_i32_16x16x64_i8 v[114:117], v[184:187], v[192:195], v[114:117]
	v_mfma_i32_16x16x64_i8 v[102:105], v[176:179], v[200:203], v[102:105]
	v_mfma_i32_16x16x64_i8 v[98:101], v[184:187], v[200:203], v[98:101]
	v_mfma_i32_16x16x64_i8 v[86:89], v[176:179], v[208:211], v[86:89]
	v_mfma_i32_16x16x64_i8 v[82:85], v[184:187], v[208:211], v[82:85]
	v_mfma_i32_16x16x64_i8 v[70:73], v[176:179], v[216:219], v[70:73]
	v_mfma_i32_16x16x64_i8 v[66:69], v[184:187], v[216:219], v[66:69]
	s_barrier
	s_add_i32 s24, s38, s29
	s_mov_b32 m0, s24
	ds_read_b128 v[188:191], v171 offset:49152
	ds_read_b128 v[192:195], v171 offset:50176
	ds_read_b128 v[196:199], v171 offset:51200
	ds_read_b128 v[200:203], v171 offset:52224
	ds_read_b128 v[204:207], v171 offset:53248
	ds_read_b128 v[208:211], v171 offset:54272
	ds_read_b128 v[212:215], v171 offset:55296
	ds_read_b128 v[216:219], v171 offset:56320
	global_load_lds_dwordx4 v148, s[98:99]
	s_add_i32 m0, s24, 0x2000
	s_add_u32 s22, s22, 0x158080
	s_addc_u32 s23, s23, 0
	s_add_i32 s24, s39, s29
	global_load_lds_dwordx4 v152, s[98:99]
	s_mov_b32 m0, s24
	s_nop 0
	global_load_lds_dwordx4 v148, s[22:23]
	s_add_i32 m0, s24, 0x2000
	s_nop 0
	global_load_lds_dwordx4 v152, s[22:23]
	s_mov_b32 m0, s36
	s_nop 0
	global_load_lds_dwordx4 v146, s[100:101]
	s_mov_b32 m0, s37
	s_nop 0
	global_load_lds_dwordx4 v150, s[100:101]
	s_waitcnt vmcnt(8)
	s_waitcnt lgkmcnt(0)
	s_barrier
	s_waitcnt lgkmcnt(0)
	v_mfma_i32_16x16x64_i8 v[62:65], v[122:125], v[188:191], v[62:65]
	v_mfma_i32_16x16x64_i8 v[58:61], v[130:133], v[188:191], v[58:61]
	v_mfma_i32_16x16x64_i8 v[46:49], v[122:125], v[196:199], v[46:49]
	v_mfma_i32_16x16x64_i8 v[42:45], v[130:133], v[196:199], v[42:45]
	v_mfma_i32_16x16x64_i8 v[30:33], v[122:125], v[204:207], v[30:33]
	v_mfma_i32_16x16x64_i8 v[26:29], v[130:133], v[204:207], v[26:29]
	v_mfma_i32_16x16x64_i8 v[14:17], v[122:125], v[212:215], v[14:17]
	v_mfma_i32_16x16x64_i8 v[10:13], v[130:133], v[212:215], v[10:13]
	v_mfma_i32_16x16x64_i8 v[62:65], v[126:129], v[192:195], v[62:65]
	v_mfma_i32_16x16x64_i8 v[58:61], v[134:137], v[192:195], v[58:61]
	v_mfma_i32_16x16x64_i8 v[46:49], v[126:129], v[200:203], v[46:49]
	v_mfma_i32_16x16x64_i8 v[42:45], v[134:137], v[200:203], v[42:45]
	v_mfma_i32_16x16x64_i8 v[30:33], v[126:129], v[208:211], v[30:33]
	v_mfma_i32_16x16x64_i8 v[26:29], v[134:137], v[208:211], v[26:29]
	v_mfma_i32_16x16x64_i8 v[14:17], v[126:129], v[216:219], v[14:17]
	v_mfma_i32_16x16x64_i8 v[10:13], v[134:137], v[216:219], v[10:13]
	v_mfma_i32_16x16x64_i8 v[54:57], v[172:175], v[188:191], v[54:57]
	v_mfma_i32_16x16x64_i8 v[50:53], v[180:183], v[188:191], v[50:53]
	v_mfma_i32_16x16x64_i8 v[38:41], v[172:175], v[196:199], v[38:41]
	v_mfma_i32_16x16x64_i8 v[34:37], v[180:183], v[196:199], v[34:37]
	v_mfma_i32_16x16x64_i8 v[22:25], v[172:175], v[204:207], v[22:25]
	v_mfma_i32_16x16x64_i8 v[18:21], v[180:183], v[204:207], v[18:21]
	v_mfma_i32_16x16x64_i8 v[6:9], v[172:175], v[212:215], v[6:9]
	v_mfma_i32_16x16x64_i8 v[2:5], v[180:183], v[212:215], v[2:5]
	v_mfma_i32_16x16x64_i8 v[54:57], v[176:179], v[192:195], v[54:57]
	v_mfma_i32_16x16x64_i8 v[50:53], v[184:187], v[192:195], v[50:53]
	v_mfma_i32_16x16x64_i8 v[38:41], v[176:179], v[200:203], v[38:41]
	v_mfma_i32_16x16x64_i8 v[34:37], v[184:187], v[200:203], v[34:37]
	v_mfma_i32_16x16x64_i8 v[22:25], v[176:179], v[208:211], v[22:25]
	v_mfma_i32_16x16x64_i8 v[18:21], v[184:187], v[208:211], v[18:21]
	v_mfma_i32_16x16x64_i8 v[6:9], v[176:179], v[216:219], v[6:9]
	v_mfma_i32_16x16x64_i8 v[2:5], v[184:187], v[216:219], v[2:5]
	s_barrier
	s_add_i32 s49, s49, 2
	s_add_u32 s20, s20, 0x100
	s_addc_u32 s21, s21, 0
	s_add_u32 s47, s47, 0x100
	s_addc_u32 s48, s48, 0
	s_cmpk_gt_u32 s49, 0x53
	s_cbranch_scc0 .LBB0_1899
	s_setprio 0
	s_and_b64 vcc, exec, s[16:17]
	s_cbranch_vccz .LBB0_1902
	s_barrier
